# next-pass prefetch in P2a: next pass's token-list entries (regs) and first two W tiles (LDS-DMA into idle A stage 1) issued before the epilogue; base v23+gate-weight prefetch+DPP
# baseline (speedup 1.0000x reference)
.LBB0_258:
	v_readlane_b32 s7, v254, 0
	s_lshr_b32 s5, s7, 2
	s_and_b32 s4, s7, 7
	s_and_b32 s5, s5, 0x3ffffff8
	s_or_b32 s4, s5, s4
	s_sub_i32 s5, 63, s4
	s_lshl_b32 s4, s4, 2
	s_add_i32 s4, s4, 0
	s_add_i32 s6, s4, 0x21400
	v_mov_b32_e32 v2, s6
	s_waitcnt lgkmcnt(0)
	s_barrier
	ds_read_b32 v2, v2
	s_lshl_b32 s5, s5, 2
	s_add_i32 s5, s5, 0
	s_add_i32 s4, s4, 0x21600
	s_add_i32 s6, s5, 0x21500
	v_mov_b32_e32 v4, s4
	s_add_i32 s4, s5, 0x21700
	v_mov_b32_e32 v3, s6
	v_mov_b32_e32 v5, s4
	ds_read_b32 v3, v3
	ds_read_b32 v4, v4
	ds_read_b32 v5, v5
	s_waitcnt lgkmcnt(3)
	v_readfirstlane_b32 s33, v2
	s_lshl_b32 s4, s33, 2
	s_add_i32 s5, 0, 0x21000
	s_add_i32 s4, s5, s4
	s_waitcnt lgkmcnt(2)
	v_readfirstlane_b32 s36, v3
	v_mov_b32_e32 v2, s4
	s_lshl_b32 s4, s36, 2
	s_add_i32 s4, s5, s4
	s_waitcnt lgkmcnt(1)
	v_readfirstlane_b32 s37, v4
	v_mov_b32_e32 v3, s4
	s_lshl_b32 s4, s37, 2
	s_add_i32 s4, s5, s4
	s_waitcnt lgkmcnt(0)
	v_readfirstlane_b32 s54, v5
	v_mov_b32_e32 v4, s4
	s_lshl_b32 s4, s54, 2
	s_add_i32 s4, s5, s4
	v_mov_b32_e32 v5, s4
	s_bfe_u32 s8, s7, 0x20003
	ds_read_b32 v2, v2
	ds_read_b32 v3, v3
	ds_read_b32 v4, v4
	ds_read_b32 v5, v5
	s_waitcnt lgkmcnt(0)
	s_barrier
	s_bitcmp0_b32 s7, 5
	s_load_dwordx4 s[12:15], s[0:1], 0x120
	s_load_dwordx2 s[6:7], s[0:1], 0x140
	s_load_dwordx2 s[16:17], s[0:1], 0x58
	s_load_dwordx2 s[18:19], s[0:1], 0xd8
	s_cselect_b64 s[4:5], -1, 0
	s_lshl_b32 s9, s8, 8
	s_add_i32 s10, s9, 0x300
	s_lshl_b32 s8, s8, 7
	s_waitcnt lgkmcnt(0)
	s_add_u32 s20, s6, s8
	s_mov_b32 s55, 0
	v_readfirstlane_b32 s56, v2
	v_readfirstlane_b32 s57, v3
	v_readfirstlane_b32 s58, v4
	v_readfirstlane_b32 s59, v5
	s_addc_u32 s21, s7, 0
	v_mov_b32_e32 v163, 0
	s_movk_i32 s60, 0xf800
	v_mov_b32_e32 v166, s10
	v_mov_b32_e32 v167, s9
	s_add_i32 s61, 0, 0x20000
	v_lshlrev_b32_e64 v244, 2, s33
	v_lshlrev_b32_e64 v245, 2, s36
	v_lshlrev_b32_e64 v246, 2, s37
	v_lshlrev_b32_e64 v247, 2, s54
	global_load_dword v244, v244, s[2:3]
	global_load_dword v245, v245, s[2:3]
	global_load_dword v246, v246, s[2:3]
	global_load_dword v247, v247, s[2:3]
	s_waitcnt vmcnt(0)
	v_readfirstlane_b32 s98, v244
	v_readfirstlane_b32 s99, v245
	v_readfirstlane_b32 s100, v246
	v_readfirstlane_b32 s101, v247
	s_nop 3
	v_writelane_b32 v253, s98, 0
	v_writelane_b32 v253, s99, 1
	v_writelane_b32 v253, s100, 2
	v_writelane_b32 v253, s101, 3
	v_writelane_b32 v253, s33, 4
	v_writelane_b32 v253, s36, 5
	v_writelane_b32 v253, s37, 6
	v_writelane_b32 v253, s54, 7
	s_nop 1
	s_mov_b32 s98, 0
	s_mov_b32 s99, -1
	v_readfirstlane_b32 s100, v0
	s_lshl_b32 s100, s100, 8
	s_and_b32 s100, s100, 0xffffc000
	s_add_i32 s67, s100, 0
	v_and_b32_e32 v240, 31, v0
	v_cmp_gt_u32_e32 vcc, 16, v240
	v_ashrrev_i32_e32 v243, 5, v0
	v_cndmask_b32_e32 v231, v166, v167, vcc
	v_lshl_add_u32 v241, v240, 4, v231
	v_lshl_or_b32 v168, v243, 13, v241
.Lmy_nxt_ap:
	s_add_i32 s99, s99, 1
	s_cmp_eq_u32 s99, 4
	s_cbranch_scc1 .Lmy_none_ap
	s_sub_i32 s100, 3, s99
	s_and_b64 vcc, s[4:5], exec
	s_cselect_b32 s100, s99, s100
	s_nop 3
	v_readlane_b32 s101, v253, s100
	s_cmp_lt_i32 s101, 1
	s_cbranch_scc1 .Lmy_nxt_ap
.Lmy_iss_ap:
	s_sub_i32 s100, 3, s99
	s_and_b64 vcc, s[4:5], exec
	s_cselect_b32 s100, s99, s100
	s_nop 3
	v_readlane_b32 s101, v253, s100
	s_add_i32 s100, s100, 4
	s_nop 3
	v_readlane_b32 s100, v253, s100
	s_sub_i32 s101, s101, s98
	s_min_i32 s101, s101, 0x200
	v_mov_b32_e32 v228, s98
	s_add_i32 s99, s101, 0x7f
	s_lshr_b32 s99, s99, 7
	s_add_i32 s101, s101, s98
	v_readfirstlane_b32 vcc_lo, v0
	s_ashr_i32 vcc_lo, vcc_lo, 2
	s_and_b32 vcc_lo, vcc_lo, -16
	s_mul_i32 vcc_lo, vcc_lo, s99
	s_add_i32 vcc_lo, vcc_lo, s98
	v_bfe_u32 v229, v0, 3, 3
	v_or_b32_e32 v229, vcc_lo, v229
	v_add_u32_e32 v232, 0, v229
	v_cmp_gt_i32_e32 vcc, s101, v232
	v_cndmask_b32_e32 v232, v228, v232, vcc
	v_lshlrev_b32_e32 v232, 2, v232
	v_add_u32_e32 v233, 8, v229
	v_cmp_gt_i32_e32 vcc, s101, v233
	v_cndmask_b32_e32 v233, v228, v233, vcc
	v_lshlrev_b32_e32 v233, 2, v233
	v_add_u32_e32 v234, 16, v229
	v_cmp_gt_i32_e32 vcc, s101, v234
	v_cndmask_b32_e32 v234, v228, v234, vcc
	v_lshlrev_b32_e32 v234, 2, v234
	v_add_u32_e32 v235, 24, v229
	v_cmp_gt_i32_e32 vcc, s101, v235
	v_cndmask_b32_e32 v235, v228, v235, vcc
	v_lshlrev_b32_e32 v235, 2, v235
	v_add_u32_e32 v236, 32, v229
	v_cmp_gt_i32_e32 vcc, s101, v236
	v_cndmask_b32_e32 v236, v228, v236, vcc
	v_lshlrev_b32_e32 v236, 2, v236
	v_add_u32_e32 v237, 40, v229
	v_cmp_gt_i32_e32 vcc, s101, v237
	v_cndmask_b32_e32 v237, v228, v237, vcc
	v_lshlrev_b32_e32 v237, 2, v237
	v_add_u32_e32 v238, 48, v229
	v_cmp_gt_i32_e32 vcc, s101, v238
	v_cndmask_b32_e32 v238, v228, v238, vcc
	v_lshlrev_b32_e32 v238, 2, v238
	v_add_u32_e32 v239, 56, v229
	v_cmp_gt_i32_e32 vcc, s101, v239
	v_cndmask_b32_e32 v239, v228, v239, vcc
	v_lshlrev_b32_e32 v239, 2, v239
	s_lshl_b32 s99, s100, 16
	s_add_u32 s98, s12, s99
	s_addc_u32 s99, s13, 0
	global_load_dword v232, v232, s[98:99]
	global_load_dword v233, v233, s[98:99]
	global_load_dword v234, v234, s[98:99]
	global_load_dword v235, v235, s[98:99]
	global_load_dword v236, v236, s[98:99]
	global_load_dword v237, v237, s[98:99]
	global_load_dword v238, v238, s[98:99]
	global_load_dword v239, v239, s[98:99]
	s_lshl_b32 s99, s100, 21
	s_add_u32 s98, s16, s99
	s_addc_u32 s99, s17, 0
	v_add_u32_e32 v230, 0x800, v168
	s_mov_b32 s100, m0
	s_add_i32 m0, s67, 0x2000
	s_nop 0
	global_load_lds_dwordx4 v168, s[98:99]
	s_add_i32 m0, s67, 0x2400
	s_nop 0
	global_load_lds_dwordx4 v230, s[98:99]
	s_add_u32 s98, s98, 0x1000
	s_addc_u32 s99, s99, 0
	s_add_i32 m0, s67, 0x2800
	s_nop 0
	global_load_lds_dwordx4 v168, s[98:99]
	s_add_i32 m0, s67, 0x2c00
	s_nop 0
	global_load_lds_dwordx4 v230, s[98:99]
	s_add_u32 s98, s98, 0x1f000
	s_addc_u32 s99, s99, 0
	s_add_i32 m0, s67, 0x3000
	s_nop 0
	global_load_lds_dwordx4 v168, s[98:99]
	s_add_i32 m0, s67, 0x3400
	s_nop 0
	global_load_lds_dwordx4 v230, s[98:99]
	s_add_u32 s98, s98, 0x1000
	s_addc_u32 s99, s99, 0
	s_add_i32 m0, s67, 0x3800
	s_nop 0
	global_load_lds_dwordx4 v168, s[98:99]
	s_add_i32 m0, s67, 0x3c00
	s_nop 0
	global_load_lds_dwordx4 v230, s[98:99]
	s_mov_b32 m0, s100
.Lmy_none_ap:
	s_mov_b32 s99, 0
	s_branch .LBB0_260

.LBB0_260:
	s_sub_i32 s8, 3, s55
	s_and_b64 s[6:7], s[4:5], exec
	s_cselect_b32 s22, s55, s8
	s_nop 3
	v_readlane_b32 s62, v253, s22
	s_cmp_eq_u32 s22, 2
	s_cselect_b64 s[8:9], -1, 0
	s_and_b64 s[6:7], s[8:9], exec
	s_cselect_b32 s23, s37, s54
	s_cmp_eq_u32 s22, 1
	s_cselect_b64 s[10:11], -1, 0
	s_and_b64 s[6:7], s[10:11], exec
	s_cselect_b32 s24, s36, s23
	s_cmp_eq_u32 s22, 0
	s_cselect_b64 s[22:23], -1, 0
	s_and_b64 s[6:7], s[22:23], exec
	s_cselect_b32 s6, s33, s24
	s_ashr_i32 s7, s6, 31
	s_cmp_lt_i32 s62, 1
	s_cbranch_scc1 .LBB0_259
	s_and_b64 s[8:9], s[8:9], exec
	s_cselect_b32 s24, s58, s59
	s_and_b64 s[8:9], s[10:11], exec
	s_cselect_b32 s10, s57, s24
	s_and_b64 s[8:9], s[22:23], exec
	s_cselect_b32 s63, s56, s10
	s_lshl_b64 s[8:9], s[6:7], 21
	s_add_u32 s22, s16, s8
	s_addc_u32 s23, s17, s9
	s_lshl_b64 s[6:7], s[6:7], 16
	s_add_u32 s24, s12, s6
	s_addc_u32 s25, s13, s7
	s_add_u32 s26, s14, s6
	s_addc_u32 s27, s15, s7
	s_add_u32 s28, s22, 0x1000
	s_addc_u32 s29, s23, 0
	s_add_u32 s30, s22, 0x20000
	s_addc_u32 s31, s23, 0
	s_add_u32 s34, s22, 0x21000
	s_addc_u32 s35, s23, 0
	s_add_u32 s38, s22, 0x40000
	s_addc_u32 s39, s23, 0
	s_add_u32 s40, s22, 0x41000
	s_addc_u32 s41, s23, 0
	s_mov_b32 s64, 0
	s_branch .LBB0_263

.LBB0_263:
	s_sub_i32 s7, s62, s64
	v_mov_b32_e32 v162, v0
	s_min_i32 s7, s7, 0x200
	s_add_i32 s8, s7, 0x7f
	v_readfirstlane_b32 s6, v162
	s_lshr_b32 s66, s8, 7
	s_ashr_i32 s8, s6, 2
	s_and_b32 s8, s8, -16
	s_mul_i32 s8, s8, s66
	s_add_i32 s8, s8, s64
	v_bfe_u32 v2, v162, 3, 3
	v_or_b32_e32 v10, s8, v2
	s_add_i32 s65, s7, s64
	v_mov_b32_e32 v11, s64
	v_cmp_gt_i32_e32 vcc, s65, v10
	v_or_b32_e32 v4, 8, v10
	v_add_u32_e32 v6, 16, v10
	v_cndmask_b32_e32 v2, v11, v10, vcc
	v_cmp_gt_i32_e32 vcc, s65, v4
	s_cmpk_gt_u32 s7, 0x80
	s_cselect_b64 s[46:47], -1, 0
	v_cndmask_b32_e32 v4, v11, v4, vcc
	v_cmp_gt_i32_e32 vcc, s65, v6
	s_and_b64 vcc, s[46:47], vcc
	v_add_u32_e32 v8, 24, v10
	v_cndmask_b32_e32 v6, v11, v6, vcc
	v_cmp_gt_i32_e32 vcc, s65, v8
	s_and_b64 vcc, s[46:47], vcc
	v_ashrrev_i32_e32 v3, 31, v2
	v_ashrrev_i32_e32 v7, 31, v6
	v_cndmask_b32_e32 v8, v11, v8, vcc
	v_lshl_add_u64 v[2:3], v[2:3], 2, s[24:25]
	v_ashrrev_i32_e32 v5, 31, v4
	v_lshl_add_u64 v[6:7], v[6:7], 2, s[24:25]
	v_ashrrev_i32_e32 v9, 31, v8
	v_lshl_add_u64 v[4:5], v[4:5], 2, s[24:25]
	v_lshl_add_u64 v[8:9], v[8:9], 2, s[24:25]
	s_cmp_lt_u32 s99, 16
	s_cbranch_scc1 .Lmy_w16_a
	s_waitcnt vmcnt(16)
	s_branch .Lmy_wd_a
.Lmy_w16_a:
	s_cmp_lt_u32 s99, 12
	s_cbranch_scc1 .Lmy_w12_a
	s_waitcnt vmcnt(12)
	s_branch .Lmy_wd_a
.Lmy_w12_a:
	s_cmp_lt_u32 s99, 8
	s_cbranch_scc1 .Lmy_w8_a
	s_waitcnt vmcnt(8)
	s_branch .Lmy_wd_a
.Lmy_w8_a:
	s_cmp_lt_u32 s99, 4
	s_cbranch_scc1 .Lmy_w4_a
	s_waitcnt vmcnt(4)
	s_branch .Lmy_wd_a

.Lmy_wd_a:
	v_mov_b32_e32 v12, v232
	v_mov_b32_e32 v13, v233
	s_nop 0
	v_mov_b32_e32 v6, v234
	s_nop 0
	v_mov_b32_e32 v7, v235
	v_add_u32_e32 v2, 32, v10
	s_cmpk_gt_u32 s7, 0x100
	s_cselect_b64 s[44:45], -1, 0
	v_cmp_gt_i32_e32 vcc, s65, v2
	s_and_b64 vcc, s[44:45], vcc
	v_add_u32_e32 v4, 40, v10
	v_cndmask_b32_e32 v2, v11, v2, vcc
	v_cmp_gt_i32_e32 vcc, s65, v4
	s_and_b64 vcc, s[44:45], vcc
	v_ashrrev_i32_e32 v3, 31, v2
	v_cndmask_b32_e32 v4, v11, v4, vcc
	v_lshl_add_u64 v[2:3], v[2:3], 2, s[24:25]
	v_ashrrev_i32_e32 v5, 31, v4
	v_lshl_add_u64 v[4:5], v[4:5], 2, s[24:25]
	v_mov_b32_e32 v8, v236
	v_mov_b32_e32 v9, v237
	v_add_u32_e32 v2, 48, v10
	s_cmpk_gt_u32 s7, 0x180
	s_cselect_b64 s[42:43], -1, 0
	v_cmp_gt_i32_e32 vcc, s65, v2
	s_and_b64 vcc, s[42:43], vcc
	v_add_u32_e32 v4, 56, v10
	v_cndmask_b32_e32 v2, v11, v2, vcc
	v_cmp_gt_i32_e32 vcc, s65, v4
	s_and_b64 vcc, s[42:43], vcc
	v_ashrrev_i32_e32 v3, 31, v2
	v_cndmask_b32_e32 v4, v11, v4, vcc
	v_lshl_add_u64 v[2:3], v[2:3], 2, s[24:25]
	v_ashrrev_i32_e32 v5, 31, v4
	v_lshl_add_u64 v[4:5], v[4:5], 2, s[24:25]
	v_mov_b32_e32 v131, v238
	v_mov_b32_e32 v130, v239
	v_and_b32_e32 v10, 31, v162
	v_and_b32_e32 v2, 7, v162
	v_bfe_u32 v3, v162, 4, 2
	v_cmp_gt_u32_e32 vcc, 16, v10
	v_bitop3_b32 v2, v3, v2, 4 bitop3:0x36
	v_ashrrev_i32_e32 v11, 5, v162
	v_cndmask_b32_e32 v15, v166, v167, vcc
	v_bitop3_b32 v14, v3, v162, 7 bitop3:0x78
	v_lshlrev_b32_e32 v132, 4, v2
	v_lshl_add_u32 v2, v10, 4, v15
	v_lshlrev_b32_e32 v133, 4, v14
	v_lshl_or_b32 v168, v11, 13, v2
	v_readfirstlane_b32 s98, v162
	s_ashr_i32 s98, s98, 6
	s_mul_i32 s98, s66, s98
	s_lshl_b32 s98, s98, 4
	v_and_or_b32 v252, v162, 15, s64
	v_add_u32_e32 v252, s98, v252
	v_lshlrev_b32_e32 v252, 2, v252
	global_load_dword v244, v252, s[26:27]
	global_load_dword v245, v252, s[26:27] offset:64
	global_load_dword v246, v252, s[26:27] offset:128
	global_load_dword v247, v252, s[26:27] offset:192
	v_lshrrev_b32_e32 v5, 4, v162
	v_lshlrev_b32_e32 v3, 11, v3
	s_lshl_b32 s6, s6, 8
	s_and_b32 s6, s6, 0xffffc000
	v_and_b32_e32 v4, 15, v162
	s_add_i32 s67, s6, 0
	s_add_i32 s68, s67, 0x400
	v_and_b32_e32 v248, 63, v162
	v_lshlrev_b32_e32 v248, 4, v248
	v_add_u32_e32 v248, s67, v248
	s_mov_b64 s[6:7], -1
	s_mov_b64 s[8:9], 0
	s_cmp_lt_i32 s66, 2
	s_mov_b64 s[10:11], 0
	s_waitcnt vmcnt(19)
	v_lshlrev_b32_e32 v2, 8, v12
	v_and_or_b32 v169, v2, s60, v133
	s_waitcnt vmcnt(18)
	v_lshlrev_b32_e32 v2, 8, v13
	v_and_or_b32 v170, v2, s60, v132
	s_waitcnt vmcnt(17)
	v_lshlrev_b32_e32 v2, 8, v6
	s_waitcnt vmcnt(16)
	v_lshlrev_b32_e32 v6, 8, v7
	v_and_or_b32 v175, v6, s60, v132
	v_and_or_b32 v174, v2, s60, v133
	s_waitcnt vmcnt(15)
	v_lshlrev_b32_e32 v2, 8, v8
	s_waitcnt vmcnt(14)
	v_lshlrev_b32_e32 v6, 8, v9
	v_and_or_b32 v177, v6, s60, v132
	v_lshlrev_b32_e32 v6, 3, v162
	v_and_or_b32 v176, v2, s60, v133
	v_lshlrev_b32_e32 v2, 10, v11
	v_and_b32_e32 v6, 24, v6
	v_add3_u32 v173, s61, v2, v6
	v_bfe_u32 v2, v162, 2, 3
	v_bitop3_b32 v134, v2, v5, 4 bitop3:0x78
	v_bfe_u32 v2, v162, 2, 2
	v_lshlrev_b32_e32 v7, 8, v2
	v_add3_u32 v3, s61, v3, v7
	v_lshrrev_b32_e32 v7, 2, v162
	v_and_or_b32 v2, v7, 4, v2
	v_lshlrev_b32_e32 v2, 5, v2
	v_add3_u32 v171, v3, v6, v2
	v_bfe_u32 v3, v162, 1, 3
	v_bitop3_b32 v3, v5, v3, 3 bitop3:0x6c
	v_lshlrev_b32_e32 v2, 7, v4
	v_lshlrev_b32_e32 v3, 4, v3
	v_add3_u32 v172, s67, v2, v3
	s_cbranch_scc1 .LBB0_275
	s_cmp_gt_i32 s66, 2
	s_cbranch_scc0 .LBB0_269
	s_cmp_eq_u32 s66, 3
	s_mov_b64 s[10:11], -1
	s_cbranch_scc0 .LBB0_270
	s_mov_b32 s6, m0
	s_mov_b32 m0, s67
	s_nop 0
	global_load_lds_dwordx4 v169, s[18:19]
	s_mov_b32 m0, s6
	s_add_i32 s52, s67, 0x800
	s_mov_b32 s6, m0
	s_mov_b32 m0, s68
	s_nop 0
	global_load_lds_dwordx4 v170, s[18:19]
	s_mov_b32 m0, s6
	s_add_i32 s53, s67, 0xc00
	s_mov_b32 s6, m0
	s_mov_b32 m0, s52
	s_nop 0
	global_load_lds_dwordx4 v174, s[18:19]
	s_mov_b32 m0, s6
	s_add_i32 s69, s67, 0x1000
	s_mov_b32 s6, m0
	s_mov_b32 m0, s53
	s_nop 0
	global_load_lds_dwordx4 v175, s[18:19]
	s_mov_b32 m0, s6
	s_add_i32 s70, s67, 0x1400
	s_mov_b32 s6, m0
	s_mov_b32 m0, s69
	s_nop 0
	global_load_lds_dwordx4 v176, s[18:19]
	s_mov_b32 m0, s6
	v_mov_b32_e32 v26, 0
	s_mov_b32 s6, m0
	s_mov_b32 m0, s70
	s_nop 0
	global_load_lds_dwordx4 v177, s[18:19]
	s_mov_b32 m0, s6
	ds_read_b128 v[228:231], v248 offset:8192
	ds_read_b128 v[232:235], v248 offset:9216
	ds_read_b128 v[236:239], v248 offset:10240
	ds_read_b128 v[240:243], v248 offset:11264
	ds_read_b128 v[60:63], v248 offset:12288
	ds_read_b128 v[64:67], v248 offset:13312
	ds_read_b128 v[68:71], v248 offset:14336
	ds_read_b128 v[72:75], v248 offset:15360
	s_waitcnt lgkmcnt(0)
	s_waitcnt vmcnt(10)
	v_mov_b32_e32 v106, v60
	v_mov_b32_e32 v107, v61
	v_mov_b32_e32 v108, v62
	v_mov_b32_e32 v109, v63
	v_mov_b32_e32 v102, v64
	v_mov_b32_e32 v103, v65
	v_mov_b32_e32 v104, v66
	v_mov_b32_e32 v105, v67
	v_mov_b32_e32 v110, v68
	v_mov_b32_e32 v111, v69
	v_mov_b32_e32 v112, v70
	v_mov_b32_e32 v113, v71
	v_mov_b32_e32 v98, v72
	v_mov_b32_e32 v99, v73
	v_mov_b32_e32 v100, v74
	v_mov_b32_e32 v101, v75
	v_xor_b32_e32 v139, 64, v172
	v_cvt_pk_bf16_f32 v2, v228, v229
	v_cvt_pk_bf16_f32 v3, v230, v231
	v_lshlrev_b32_e32 v4, 5, v134
	v_add_u32_e32 v135, v173, v4
	v_xor_b32_e32 v5, 32, v4
	ds_write_b64 v135, v[2:3]
	v_cvt_pk_bf16_f32 v2, v232, v233
	v_cvt_pk_bf16_f32 v3, v234, v235
	v_add_u32_e32 v136, v173, v5
	v_xor_b32_e32 v5, 64, v4
	ds_write_b64 v136, v[2:3] offset:256
	v_cvt_pk_bf16_f32 v2, v236, v237
	v_cvt_pk_bf16_f32 v3, v238, v239
	v_add_u32_e32 v137, v173, v5
	v_xor_b32_e32 v4, 0x60, v4
	ds_write_b64 v137, v[2:3] offset:512
	v_cvt_pk_bf16_f32 v2, v240, v241
	v_cvt_pk_bf16_f32 v3, v242, v243
	v_add_u32_e32 v138, v173, v4
	ds_write_b64 v138, v[2:3] offset:768
	global_load_dwordx4 v[122:125], v168, s[38:39]
	global_load_dwordx4 v[118:121], v168, s[38:39] offset:2048
	global_load_dwordx4 v[126:129], v168, s[40:41]
	global_load_dwordx4 v[114:117], v168, s[40:41] offset:2048
	s_waitcnt lgkmcnt(0)
	s_barrier
	v_add_u32_e32 v2, 0x2000, v172
	s_add_i32 s71, s67, 0x2000
	v_xor_b32_e32 v140, 64, v2
	v_xor_b32_e32 v141, 32, v171
	v_xor_b32_e32 v142, 64, v171
	v_xor_b32_e32 v143, 0x60, v171
	v_xor_b32_e32 v144, 0x80, v171
	v_xor_b32_e32 v145, 0xa0, v171
	v_xor_b32_e32 v146, 0xc0, v171
	s_add_i32 s72, s67, 0x2400
	v_xor_b32_e32 v147, 0xe0, v171
	s_add_i32 s73, s67, 0x2800
	s_add_i32 s74, s67, 0x2c00
	s_add_i32 s75, s67, 0x3000
	s_add_i32 s76, s67, 0x3400
	s_mov_b32 s50, 0
	s_mov_b64 s[10:11], 0
	v_mov_b32_e32 v27, v26
	v_mov_b32_e32 v28, v26
	v_mov_b32_e32 v29, v26
	v_mov_b32_e32 v2, v26
	v_mov_b32_e32 v3, v26
	v_mov_b32_e32 v4, v26
	v_mov_b32_e32 v5, v26
	v_mov_b32_e32 v10, v26
	v_mov_b32_e32 v11, v26
	v_mov_b32_e32 v12, v26
	v_mov_b32_e32 v13, v26
	v_mov_b32_e32 v50, v26
	v_mov_b32_e32 v51, v26
	v_mov_b32_e32 v52, v26
	v_mov_b32_e32 v53, v26
	v_mov_b32_e32 v14, v26
	v_mov_b32_e32 v15, v26
	v_mov_b32_e32 v16, v26
	v_mov_b32_e32 v17, v26
	v_mov_b32_e32 v30, v26
	v_mov_b32_e32 v31, v26
	v_mov_b32_e32 v32, v26
	v_mov_b32_e32 v33, v26
	v_mov_b32_e32 v66, v26
	v_mov_b32_e32 v67, v26
	v_mov_b32_e32 v68, v26
	v_mov_b32_e32 v69, v26
	v_mov_b32_e32 v34, v26
	v_mov_b32_e32 v35, v26
	v_mov_b32_e32 v36, v26
	v_mov_b32_e32 v37, v26
	v_mov_b32_e32 v62, v26
	v_mov_b32_e32 v63, v26
	v_mov_b32_e32 v64, v26
	v_mov_b32_e32 v65, v26
	v_mov_b32_e32 v82, v26
	v_mov_b32_e32 v83, v26
	v_mov_b32_e32 v84, v26
	v_mov_b32_e32 v85, v26
	v_mov_b32_e32 v54, v26
	v_mov_b32_e32 v55, v26
	v_mov_b32_e32 v56, v26
	v_mov_b32_e32 v57, v26
	v_mov_b32_e32 v86, v26
	v_mov_b32_e32 v87, v26
	v_mov_b32_e32 v88, v26
	v_mov_b32_e32 v89, v26
	v_mov_b32_e32 v22, v26
	v_mov_b32_e32 v23, v26
	v_mov_b32_e32 v24, v26
	v_mov_b32_e32 v25, v26
	v_mov_b32_e32 v6, v26
	v_mov_b32_e32 v7, v26
	v_mov_b32_e32 v8, v26
	v_mov_b32_e32 v9, v26
	v_mov_b32_e32 v42, v26
	v_mov_b32_e32 v43, v26
	v_mov_b32_e32 v44, v26
	v_mov_b32_e32 v45, v26
	v_mov_b32_e32 v38, v26
	v_mov_b32_e32 v39, v26
	v_mov_b32_e32 v40, v26
	v_mov_b32_e32 v41, v26
	v_mov_b32_e32 v18, v26
	v_mov_b32_e32 v19, v26
	v_mov_b32_e32 v20, v26
	v_mov_b32_e32 v21, v26
	v_mov_b32_e32 v70, v26
	v_mov_b32_e32 v71, v26
	v_mov_b32_e32 v72, v26
	v_mov_b32_e32 v73, v26
	v_mov_b32_e32 v58, v26
	v_mov_b32_e32 v59, v26
	v_mov_b32_e32 v60, v26
	v_mov_b32_e32 v61, v26
	v_mov_b32_e32 v46, v26
	v_mov_b32_e32 v47, v26
	v_mov_b32_e32 v48, v26
	v_mov_b32_e32 v49, v26
	v_mov_b32_e32 v90, v26
	v_mov_b32_e32 v91, v26
	v_mov_b32_e32 v92, v26
	v_mov_b32_e32 v93, v26
	v_mov_b32_e32 v78, v26
	v_mov_b32_e32 v79, v26
	v_mov_b32_e32 v80, v26
	v_mov_b32_e32 v81, v26
	v_mov_b32_e32 v74, v26
	v_mov_b32_e32 v75, v26
	v_mov_b32_e32 v76, v26
	v_mov_b32_e32 v77, v26
	v_mov_b32_e32 v94, v26
	v_mov_b32_e32 v95, v26
	v_mov_b32_e32 v96, v26
	v_mov_b32_e32 v97, v26

.LBB0_271:
	s_mov_b32 s6, m0
	s_mov_b32 m0, s67
	s_nop 0
	global_load_lds_dwordx4 v169, s[18:19]
	s_mov_b32 m0, s6
	s_add_i32 s69, s67, 0x800
	s_mov_b32 s6, m0
	s_mov_b32 m0, s68
	s_nop 0
	global_load_lds_dwordx4 v170, s[18:19]
	s_mov_b32 m0, s6
	s_add_i32 s70, s67, 0xc00
	s_mov_b32 s6, m0
	s_mov_b32 m0, s69
	s_nop 0
	global_load_lds_dwordx4 v174, s[18:19]
	s_mov_b32 m0, s6
	v_xor_b32_e32 v102, 64, v172
	s_mov_b32 s6, m0
	s_mov_b32 m0, s70
	s_nop 0
	global_load_lds_dwordx4 v175, s[18:19]
	s_mov_b32 m0, s6
	ds_read_b128 v[228:231], v248 offset:8192
	ds_read_b128 v[232:235], v248 offset:9216
	ds_read_b128 v[236:239], v248 offset:10240
	ds_read_b128 v[240:243], v248 offset:11264
	ds_read_b128 v[60:63], v248 offset:12288
	ds_read_b128 v[64:67], v248 offset:13312
	ds_read_b128 v[68:71], v248 offset:14336
	ds_read_b128 v[72:75], v248 offset:15360
	s_waitcnt lgkmcnt(0)
	s_waitcnt vmcnt(8)
	v_mov_b32_e32 v38, v60
	v_mov_b32_e32 v39, v61
	v_mov_b32_e32 v40, v62
	v_mov_b32_e32 v41, v63
	v_mov_b32_e32 v26, v64
	v_mov_b32_e32 v27, v65
	v_mov_b32_e32 v28, v66
	v_mov_b32_e32 v29, v67
	v_mov_b32_e32 v50, v68
	v_mov_b32_e32 v51, v69
	v_mov_b32_e32 v52, v70
	v_mov_b32_e32 v53, v71
	v_mov_b32_e32 v22, v72
	v_mov_b32_e32 v23, v73
	v_mov_b32_e32 v24, v74
	v_mov_b32_e32 v25, v75
	s_add_i32 s71, s67, 0x2000
	v_cvt_pk_bf16_f32 v2, v228, v229
	v_cvt_pk_bf16_f32 v3, v230, v231
	v_lshlrev_b32_e32 v4, 5, v134
	v_add_u32_e32 v98, v173, v4
	v_xor_b32_e32 v5, 32, v4
	ds_write_b64 v98, v[2:3]
	v_cvt_pk_bf16_f32 v2, v232, v233
	v_cvt_pk_bf16_f32 v3, v234, v235
	v_add_u32_e32 v99, v173, v5
	v_xor_b32_e32 v5, 64, v4
	ds_write_b64 v99, v[2:3] offset:256
	v_cvt_pk_bf16_f32 v2, v236, v237
	v_cvt_pk_bf16_f32 v3, v238, v239
	v_add_u32_e32 v100, v173, v5
	v_xor_b32_e32 v4, 0x60, v4
	ds_write_b64 v100, v[2:3] offset:512
	v_cvt_pk_bf16_f32 v2, v240, v241
	v_cvt_pk_bf16_f32 v3, v242, v243
	v_add_u32_e32 v101, v173, v4
	ds_write_b64 v101, v[2:3] offset:768
	global_load_dwordx4 v[78:81], v168, s[38:39]
	global_load_dwordx4 v[66:69], v168, s[38:39] offset:2048
	global_load_dwordx4 v[82:85], v168, s[40:41]
	global_load_dwordx4 v[58:61], v168, s[40:41] offset:2048
	s_waitcnt lgkmcnt(0)
	s_barrier
	v_add_u32_e32 v2, 0x2000, v172
	v_xor_b32_e32 v103, 64, v2
	v_mov_b32_e32 v2, 0
	v_xor_b32_e32 v104, 32, v171
	v_xor_b32_e32 v105, 64, v171
	v_xor_b32_e32 v106, 0x60, v171
	v_xor_b32_e32 v107, 0x80, v171
	v_xor_b32_e32 v108, 0xa0, v171
	v_xor_b32_e32 v109, 0xc0, v171
	s_add_i32 s72, s67, 0x2400
	v_xor_b32_e32 v110, 0xe0, v171
	s_add_i32 s73, s67, 0x2800
	s_add_i32 s74, s67, 0x2c00
	s_mov_b32 s52, 0
	s_mov_b64 s[48:49], 0
	v_mov_b32_e32 v3, v2
	v_mov_b32_e32 v4, v2
	v_mov_b32_e32 v5, v2
	v_mov_b32_e32 v10, v2
	v_mov_b32_e32 v11, v2
	v_mov_b32_e32 v12, v2
	v_mov_b32_e32 v13, v2
	v_mov_b32_e32 v14, v2
	v_mov_b32_e32 v15, v2
	v_mov_b32_e32 v16, v2
	v_mov_b32_e32 v17, v2
	v_mov_b32_e32 v30, v2
	v_mov_b32_e32 v31, v2
	v_mov_b32_e32 v32, v2
	v_mov_b32_e32 v33, v2
	v_mov_b32_e32 v34, v2
	v_mov_b32_e32 v35, v2
	v_mov_b32_e32 v36, v2
	v_mov_b32_e32 v37, v2
	v_mov_b32_e32 v62, v2
	v_mov_b32_e32 v63, v2
	v_mov_b32_e32 v64, v2
	v_mov_b32_e32 v65, v2
	v_mov_b32_e32 v54, v2
	v_mov_b32_e32 v55, v2
	v_mov_b32_e32 v56, v2
	v_mov_b32_e32 v57, v2
	v_mov_b32_e32 v86, v2
	v_mov_b32_e32 v87, v2
	v_mov_b32_e32 v88, v2
	v_mov_b32_e32 v89, v2
	v_mov_b32_e32 v6, v2
	v_mov_b32_e32 v7, v2
	v_mov_b32_e32 v8, v2
	v_mov_b32_e32 v9, v2
	v_mov_b32_e32 v42, v2
	v_mov_b32_e32 v43, v2
	v_mov_b32_e32 v44, v2
	v_mov_b32_e32 v45, v2
	v_mov_b32_e32 v18, v2
	v_mov_b32_e32 v19, v2
	v_mov_b32_e32 v20, v2
	v_mov_b32_e32 v21, v2
	v_mov_b32_e32 v70, v2
	v_mov_b32_e32 v71, v2
	v_mov_b32_e32 v72, v2
	v_mov_b32_e32 v73, v2
	v_mov_b32_e32 v46, v2
	v_mov_b32_e32 v47, v2
	v_mov_b32_e32 v48, v2
	v_mov_b32_e32 v49, v2
	v_mov_b32_e32 v90, v2
	v_mov_b32_e32 v91, v2
	v_mov_b32_e32 v92, v2
	v_mov_b32_e32 v93, v2
	v_mov_b32_e32 v74, v2
	v_mov_b32_e32 v75, v2
	v_mov_b32_e32 v76, v2
	v_mov_b32_e32 v77, v2
	v_mov_b32_e32 v94, v2
	v_mov_b32_e32 v95, v2
	v_mov_b32_e32 v96, v2
	v_mov_b32_e32 v97, v2

.LBB0_277:
	v_mov_b32_e32 v125, 0
	v_lshlrev_b32_e32 v98, 5, v134
	v_add_u32_e32 v99, 0x2000, v172
	s_andn2_b64 vcc, exec, s[10:11]
	v_xor_b32_e32 v178, 64, v172
	v_xor_b32_e32 v179, 32, v171
	v_xor_b32_e32 v180, 64, v171
	v_xor_b32_e32 v181, 0x60, v171
	v_xor_b32_e32 v182, 0x80, v171
	v_xor_b32_e32 v183, 0xa0, v171
	v_xor_b32_e32 v184, 0xc0, v171
	v_xor_b32_e32 v185, 0xe0, v171
	v_add_u32_e32 v186, v173, v98
	v_xor_b32_e32 v190, 32, v98
	v_xor_b32_e32 v189, 64, v98
	v_xor_b32_e32 v188, 0x60, v98
	v_xor_b32_e32 v187, 64, v99
	v_mov_b32_e32 v124, v125
	v_mov_b32_e32 v123, v125
	v_mov_b32_e32 v122, v125
	v_mov_b32_e32 v117, v125
	v_mov_b32_e32 v116, v125
	v_mov_b32_e32 v115, v125
	v_mov_b32_e32 v114, v125
	v_mov_b32_e32 v109, v125
	v_mov_b32_e32 v108, v125
	v_mov_b32_e32 v107, v125
	v_mov_b32_e32 v106, v125
	v_mov_b32_e32 v105, v125
	v_mov_b32_e32 v104, v125
	v_mov_b32_e32 v103, v125
	v_mov_b32_e32 v102, v125
	v_mov_b32_e32 v129, v125
	v_mov_b32_e32 v128, v125
	v_mov_b32_e32 v127, v125
	v_mov_b32_e32 v126, v125
	v_mov_b32_e32 v121, v125
	v_mov_b32_e32 v120, v125
	v_mov_b32_e32 v119, v125
	v_mov_b32_e32 v118, v125
	v_mov_b32_e32 v113, v125
	v_mov_b32_e32 v112, v125
	v_mov_b32_e32 v111, v125
	v_mov_b32_e32 v110, v125
	v_mov_b32_e32 v101, v125
	v_mov_b32_e32 v100, v125
	v_mov_b32_e32 v99, v125
	v_mov_b32_e32 v98, v125
	s_cbranch_vccnz .LBB0_281
	s_waitcnt vmcnt(13)
	v_lshlrev_b32_e32 v2, 8, v131
	v_and_or_b32 v191, v2, s60, v133
	s_waitcnt vmcnt(12)
	v_lshlrev_b32_e32 v2, 8, v130
	v_and_or_b32 v192, v2, s60, v132
	s_mov_b32 s6, m0
	s_mov_b32 m0, s67
	s_nop 0
	global_load_lds_dwordx4 v169, s[18:19]
	s_mov_b32 m0, s6
	s_add_i32 s50, s67, 0x800
	s_mov_b32 s6, m0
	s_mov_b32 m0, s68
	s_nop 0
	global_load_lds_dwordx4 v170, s[18:19]
	s_mov_b32 m0, s6
	s_add_i32 s51, s67, 0xc00
	s_mov_b32 s6, m0
	s_mov_b32 m0, s50
	s_nop 0
	global_load_lds_dwordx4 v174, s[18:19]
	s_mov_b32 m0, s6
	s_add_i32 s52, s67, 0x1000
	s_mov_b32 s6, m0
	s_mov_b32 m0, s51
	s_nop 0
	global_load_lds_dwordx4 v175, s[18:19]
	s_mov_b32 m0, s6
	s_add_i32 s53, s67, 0x1400
	s_mov_b32 s6, m0
	s_mov_b32 m0, s52
	s_nop 0
	global_load_lds_dwordx4 v176, s[18:19]
	s_mov_b32 m0, s6
	s_add_i32 s69, s67, 0x1800
	s_mov_b32 s6, m0
	s_mov_b32 m0, s53
	s_nop 0
	global_load_lds_dwordx4 v177, s[18:19]
	s_mov_b32 m0, s6
	s_add_i32 s70, s67, 0x1c00
	s_mov_b32 s6, m0
	s_mov_b32 m0, s69
	s_nop 0
	global_load_lds_dwordx4 v191, s[18:19]
	s_mov_b32 m0, s6
	v_add_u32_e32 v193, v173, v190
	s_mov_b32 s6, m0
	s_mov_b32 m0, s70
	s_nop 0
	global_load_lds_dwordx4 v192, s[18:19]
	s_mov_b32 m0, s6
	ds_read_b128 v[228:231], v248 offset:8192
	ds_read_b128 v[232:235], v248 offset:9216
	ds_read_b128 v[236:239], v248 offset:10240
	ds_read_b128 v[240:243], v248 offset:11264
	ds_read_b128 v[60:63], v248 offset:12288
	ds_read_b128 v[64:67], v248 offset:13312
	ds_read_b128 v[68:71], v248 offset:14336
	ds_read_b128 v[72:75], v248 offset:15360
	s_waitcnt lgkmcnt(0)
	s_waitcnt vmcnt(12)
	v_mov_b32_e32 v138, v60
	v_mov_b32_e32 v139, v61
	v_mov_b32_e32 v140, v62
	v_mov_b32_e32 v141, v63
	v_mov_b32_e32 v134, v64
	v_mov_b32_e32 v135, v65
	v_mov_b32_e32 v136, v66
	v_mov_b32_e32 v137, v67
	v_mov_b32_e32 v142, v68
	v_mov_b32_e32 v143, v69
	v_mov_b32_e32 v144, v70
	v_mov_b32_e32 v145, v71
	v_mov_b32_e32 v130, v72
	v_mov_b32_e32 v131, v73
	v_mov_b32_e32 v132, v74
	v_mov_b32_e32 v133, v75
	v_add_u32_e32 v194, v173, v189
	v_cvt_pk_bf16_f32 v2, v228, v229
	v_cvt_pk_bf16_f32 v3, v230, v231
	ds_write_b64 v186, v[2:3]
	v_cvt_pk_bf16_f32 v2, v232, v233
	v_cvt_pk_bf16_f32 v3, v234, v235
	ds_write_b64 v193, v[2:3] offset:256
	v_cvt_pk_bf16_f32 v2, v236, v237
	v_cvt_pk_bf16_f32 v3, v238, v239
	ds_write_b64 v194, v[2:3] offset:512
	v_cvt_pk_bf16_f32 v2, v240, v241
	v_cvt_pk_bf16_f32 v3, v242, v243
	v_add_u32_e32 v195, v173, v188
	ds_write_b64 v195, v[2:3] offset:768
	global_load_dwordx4 v[154:157], v168, s[38:39]
	global_load_dwordx4 v[150:153], v168, s[38:39] offset:2048
	global_load_dwordx4 v[158:161], v168, s[40:41]
	global_load_dwordx4 v[146:149], v168, s[40:41] offset:2048
	s_waitcnt lgkmcnt(0)
	s_barrier
	v_mov_b32_e32 v98, 0
	s_add_i32 s71, s67, 0x2000
	s_add_i32 s72, s67, 0x2400
	s_add_i32 s73, s67, 0x2800
	s_add_i32 s74, s67, 0x2c00
	s_add_i32 s75, s67, 0x3000
	s_add_i32 s76, s67, 0x3400
	s_add_i32 s77, s67, 0x3800
	s_add_i32 s78, s67, 0x3c00
	s_mov_b32 s48, 0
	s_mov_b64 s[8:9], 0
	v_mov_b32_e32 v99, v98
	v_mov_b32_e32 v100, v98
	v_mov_b32_e32 v101, v98
	v_mov_b32_e32 v26, v98
	v_mov_b32_e32 v27, v98
	v_mov_b32_e32 v28, v98
	v_mov_b32_e32 v29, v98
	v_mov_b32_e32 v2, v98
	v_mov_b32_e32 v3, v98
	v_mov_b32_e32 v4, v98
	v_mov_b32_e32 v5, v98
	v_mov_b32_e32 v10, v98
	v_mov_b32_e32 v11, v98
	v_mov_b32_e32 v12, v98
	v_mov_b32_e32 v13, v98
	v_mov_b32_e32 v110, v98
	v_mov_b32_e32 v111, v98
	v_mov_b32_e32 v112, v98
	v_mov_b32_e32 v113, v98
	v_mov_b32_e32 v50, v98
	v_mov_b32_e32 v51, v98
	v_mov_b32_e32 v52, v98
	v_mov_b32_e32 v53, v98
	v_mov_b32_e32 v14, v98
	v_mov_b32_e32 v15, v98
	v_mov_b32_e32 v16, v98
	v_mov_b32_e32 v17, v98
	v_mov_b32_e32 v30, v98
	v_mov_b32_e32 v31, v98
	v_mov_b32_e32 v32, v98
	v_mov_b32_e32 v33, v98
	v_mov_b32_e32 v118, v98
	v_mov_b32_e32 v119, v98
	v_mov_b32_e32 v120, v98
	v_mov_b32_e32 v121, v98
	v_mov_b32_e32 v66, v98
	v_mov_b32_e32 v67, v98
	v_mov_b32_e32 v68, v98
	v_mov_b32_e32 v69, v98
	v_mov_b32_e32 v34, v98
	v_mov_b32_e32 v35, v98
	v_mov_b32_e32 v36, v98
	v_mov_b32_e32 v37, v98
	v_mov_b32_e32 v62, v98
	v_mov_b32_e32 v63, v98
	v_mov_b32_e32 v64, v98
	v_mov_b32_e32 v65, v98
	v_mov_b32_e32 v126, v98
	v_mov_b32_e32 v127, v98
	v_mov_b32_e32 v128, v98
	v_mov_b32_e32 v129, v98
	v_mov_b32_e32 v82, v98
	v_mov_b32_e32 v83, v98
	v_mov_b32_e32 v84, v98
	v_mov_b32_e32 v85, v98
	v_mov_b32_e32 v54, v98
	v_mov_b32_e32 v55, v98
	v_mov_b32_e32 v56, v98
	v_mov_b32_e32 v57, v98
	v_mov_b32_e32 v86, v98
	v_mov_b32_e32 v87, v98
	v_mov_b32_e32 v88, v98
	v_mov_b32_e32 v89, v98
	v_mov_b32_e32 v102, v98
	v_mov_b32_e32 v103, v98
	v_mov_b32_e32 v104, v98
	v_mov_b32_e32 v105, v98
	v_mov_b32_e32 v22, v98
	v_mov_b32_e32 v23, v98
	v_mov_b32_e32 v24, v98
	v_mov_b32_e32 v25, v98
	v_mov_b32_e32 v6, v98
	v_mov_b32_e32 v7, v98
	v_mov_b32_e32 v8, v98
	v_mov_b32_e32 v9, v98
	v_mov_b32_e32 v42, v98
	v_mov_b32_e32 v43, v98
	v_mov_b32_e32 v44, v98
	v_mov_b32_e32 v45, v98
	v_mov_b32_e32 v106, v98
	v_mov_b32_e32 v107, v98
	v_mov_b32_e32 v108, v98
	v_mov_b32_e32 v109, v98
	v_mov_b32_e32 v38, v98
	v_mov_b32_e32 v39, v98
	v_mov_b32_e32 v40, v98
	v_mov_b32_e32 v41, v98
	v_mov_b32_e32 v18, v98
	v_mov_b32_e32 v19, v98
	v_mov_b32_e32 v20, v98
	v_mov_b32_e32 v21, v98
	v_mov_b32_e32 v70, v98
	v_mov_b32_e32 v71, v98
	v_mov_b32_e32 v72, v98
	v_mov_b32_e32 v73, v98
	v_mov_b32_e32 v114, v98
	v_mov_b32_e32 v115, v98
	v_mov_b32_e32 v116, v98
	v_mov_b32_e32 v117, v98
	v_mov_b32_e32 v58, v98
	v_mov_b32_e32 v59, v98
	v_mov_b32_e32 v60, v98
	v_mov_b32_e32 v61, v98
	v_mov_b32_e32 v46, v98
	v_mov_b32_e32 v47, v98
	v_mov_b32_e32 v48, v98
	v_mov_b32_e32 v49, v98
	v_mov_b32_e32 v90, v98
	v_mov_b32_e32 v91, v98
	v_mov_b32_e32 v92, v98
	v_mov_b32_e32 v93, v98
	v_mov_b32_e32 v122, v98
	v_mov_b32_e32 v123, v98
	v_mov_b32_e32 v124, v98
	v_mov_b32_e32 v125, v98
	v_mov_b32_e32 v78, v98
	v_mov_b32_e32 v79, v98
	v_mov_b32_e32 v80, v98
	v_mov_b32_e32 v81, v98
	v_mov_b32_e32 v74, v98
	v_mov_b32_e32 v75, v98
	v_mov_b32_e32 v76, v98
	v_mov_b32_e32 v77, v98
	v_mov_b32_e32 v94, v98
	v_mov_b32_e32 v95, v98
	v_mov_b32_e32 v96, v98
	v_mov_b32_e32 v97, v98

.LBB0_281:
	s_and_b64 vcc, exec, s[8:9]
	s_cbranch_vccz .LBB0_285
	s_mov_b32 s6, m0
	s_mov_b32 m0, s67
	s_nop 0
	global_load_lds_dwordx4 v169, s[18:19]
	s_mov_b32 m0, s6
	v_add_u32_e32 v47, v173, v189
	s_mov_b32 s6, m0
	s_mov_b32 m0, s68
	s_nop 0
	global_load_lds_dwordx4 v170, s[18:19]
	s_mov_b32 m0, s6
	ds_read_b128 v[228:231], v248 offset:8192
	ds_read_b128 v[232:235], v248 offset:9216
	ds_read_b128 v[236:239], v248 offset:10240
	ds_read_b128 v[240:243], v248 offset:11264
	ds_read_b128 v[60:63], v248 offset:12288
	ds_read_b128 v[64:67], v248 offset:13312
	ds_read_b128 v[68:71], v248 offset:14336
	ds_read_b128 v[72:75], v248 offset:15360
	s_waitcnt lgkmcnt(0)
	s_waitcnt vmcnt(6)
	v_mov_b32_e32 v18, v60
	v_mov_b32_e32 v19, v61
	v_mov_b32_e32 v20, v62
	v_mov_b32_e32 v21, v63
	v_mov_b32_e32 v6, v64
	v_mov_b32_e32 v7, v65
	v_mov_b32_e32 v8, v66
	v_mov_b32_e32 v9, v67
	v_mov_b32_e32 v14, v68
	v_mov_b32_e32 v15, v69
	v_mov_b32_e32 v16, v70
	v_mov_b32_e32 v17, v71
	v_mov_b32_e32 v2, v72
	v_mov_b32_e32 v3, v73
	v_mov_b32_e32 v4, v74
	v_mov_b32_e32 v5, v75
	v_add_u32_e32 v46, v173, v190
	v_cvt_pk_bf16_f32 v10, v228, v229
	v_cvt_pk_bf16_f32 v11, v230, v231
	ds_write_b64 v186, v[10:11]
	v_cvt_pk_bf16_f32 v10, v236, v237
	v_cvt_pk_bf16_f32 v11, v238, v239
	v_cvt_pk_bf16_f32 v12, v232, v233
	v_cvt_pk_bf16_f32 v13, v234, v235
	ds_write_b64 v47, v[10:11] offset:512
	v_cvt_pk_bf16_f32 v10, v240, v241
	v_cvt_pk_bf16_f32 v11, v242, v243
	v_add_u32_e32 v48, v173, v188
	ds_write_b64 v46, v[12:13] offset:256
	ds_write_b64 v48, v[10:11] offset:768
	global_load_dwordx4 v[38:41], v168, s[38:39]
	global_load_dwordx4 v[26:29], v168, s[38:39] offset:2048
	global_load_dwordx4 v[34:37], v168, s[40:41]
	global_load_dwordx4 v[22:25], v168, s[40:41] offset:2048
	s_waitcnt lgkmcnt(0)
	s_barrier
	v_mov_b32_e32 v10, 0
	s_add_i32 s48, s67, 0x2000
	s_add_i32 s49, s67, 0x2400
	s_mov_b32 s50, 0
	s_mov_b64 s[8:9], 0
	v_mov_b32_e32 v11, v10
	v_mov_b32_e32 v12, v10
	v_mov_b32_e32 v13, v10
	v_mov_b32_e32 v30, v10
	v_mov_b32_e32 v31, v10
	v_mov_b32_e32 v32, v10
	v_mov_b32_e32 v33, v10
	v_mov_b32_e32 v62, v10
	v_mov_b32_e32 v63, v10
	v_mov_b32_e32 v64, v10
	v_mov_b32_e32 v65, v10
	v_mov_b32_e32 v86, v10
	v_mov_b32_e32 v87, v10
	v_mov_b32_e32 v88, v10
	v_mov_b32_e32 v89, v10
	v_mov_b32_e32 v42, v10
	v_mov_b32_e32 v43, v10
	v_mov_b32_e32 v44, v10
	v_mov_b32_e32 v45, v10
	v_mov_b32_e32 v70, v10
	v_mov_b32_e32 v71, v10
	v_mov_b32_e32 v72, v10
	v_mov_b32_e32 v73, v10
	v_mov_b32_e32 v90, v10
	v_mov_b32_e32 v91, v10
	v_mov_b32_e32 v92, v10
	v_mov_b32_e32 v93, v10
	v_mov_b32_e32 v94, v10
	v_mov_b32_e32 v95, v10
	v_mov_b32_e32 v96, v10
	v_mov_b32_e32 v97, v10

.LBB0_285:
	s_add_i32 s98, s64, 0x200
	s_cmp_lt_i32 s98, s62
	s_mov_b32 s99, s55
	s_cbranch_scc1 .Lmy_iss_ae
	s_mov_b32 s98, 0

.Lmy_none_ae:
	s_mov_b32 s99, 0
	s_nop 0
	v_readfirstlane_b32 s6, v162
	s_ashr_i32 s6, s6, 6
	s_mul_i32 s66, s66, s6
	v_and_or_b32 v131, v162, 15, s64
	v_lshrrev_b32_e32 v130, 2, v162
	s_lshl_b32 s50, s66, 4
	v_and_b32_e32 v130, 12, v130
	v_add_u32_e32 v132, s50, v131
	v_cmp_gt_i32_e32 vcc, s65, v132
	v_lshlrev_b32_e32 v162, 1, v130
	s_and_saveexec_b64 s[48:49], vcc
	s_cbranch_execz .LBB0_287
	s_add_i32 s99, s99, 4
	v_ashrrev_i32_e32 v133, 31, v132
	v_lshl_add_u64 v[134:135], v[132:133], 2, s[26:27]
	v_mul_f32_e32 v134, 0xbfb8aa3b, v94
	v_mul_f32_e32 v135, 0xbfb8aa3b, v95
	v_exp_f32_e32 v134, v134
	v_exp_f32_e32 v135, v135
	v_mul_f32_e32 v136, 0xbfb8aa3b, v96
	v_mul_f32_e32 v137, 0xbfb8aa3b, v97
	v_exp_f32_e32 v136, v136
	v_exp_f32_e32 v137, v137
	v_pk_add_f32 v[134:135], v[134:135], 1.0 op_sel_hi:[1,0]
	v_mul_f32_e32 v138, 0xbfb8aa3b, v90
	v_pk_add_f32 v[136:137], v[136:137], 1.0 op_sel_hi:[1,0]
	v_mul_f32_e32 v139, 0xbfb8aa3b, v91
	v_exp_f32_e32 v138, v138
	v_exp_f32_e32 v139, v139
	v_rcp_f32_e32 v140, v135
	s_nop 0
	v_mul_f32_e32 v95, v95, v140
	v_rcp_f32_e32 v135, v134
	s_nop 0
	v_mul_f32_e32 v94, v94, v135
	v_pk_mul_f32 v[86:87], v[86:87], v[94:95]
	v_pk_add_f32 v[138:139], v[138:139], 1.0 op_sel_hi:[1,0]
	v_rcp_f32_e32 v134, v137
	s_nop 0
	v_mul_f32_e32 v95, v97, v134
	v_rcp_f32_e32 v94, v136
	s_nop 0
	v_mul_f32_e32 v94, v96, v94
	v_add_u32_e32 v132, s63, v132
	v_pk_mul_f32 v[88:89], v[88:89], v[94:95]
	v_ashrrev_i32_e32 v133, 31, v132
	v_lshlrev_b64 v[132:133], 9, v[132:133]
	v_lshl_add_u64 v[132:133], s[20:21], 0, v[132:133]
	v_mov_b32_e32 v130, v244
	v_pk_mul_f32 v[86:87], v[86:87], v[130:131] op_sel_hi:[1,0]
	v_pk_mul_f32 v[88:89], v[88:89], v[130:131] op_sel_hi:[1,0]
	v_lshl_add_u64 v[132:133], v[132:133], 0, v[162:163]
	v_cvt_pk_bf16_f32 v86, v86, v87
	v_cvt_pk_bf16_f32 v87, v88, v89
	global_store_dwordx2 v[132:133], v[86:87], off
	v_rcp_f32_e32 v86, v139
	s_nop 0
	v_mul_f32_e32 v87, v91, v86
	v_mul_f32_e32 v88, 0xbfb8aa3b, v92
	v_mul_f32_e32 v89, 0xbfb8aa3b, v93
	v_exp_f32_e32 v88, v88
	v_exp_f32_e32 v89, v89
	v_rcp_f32_e32 v86, v138
	s_nop 0
	v_mul_f32_e32 v86, v90, v86
	v_pk_mul_f32 v[62:63], v[62:63], v[86:87]
	v_pk_add_f32 v[88:89], v[88:89], 1.0 op_sel_hi:[1,0]
	v_pk_mul_f32 v[62:63], v[62:63], v[130:131] op_sel_hi:[1,0]
	v_cvt_pk_bf16_f32 v62, v62, v63
	v_rcp_f32_e32 v63, v89
	s_nop 0
	v_mul_f32_e32 v87, v93, v63
	v_mul_f32_e32 v89, 0xbfb8aa3b, v70
	v_exp_f32_e32 v90, v89
	v_mul_f32_e32 v89, 0xbfb8aa3b, v71
	v_exp_f32_e32 v91, v89
	v_rcp_f32_e32 v63, v88
	s_nop 0
	v_mul_f32_e32 v86, v92, v63
	v_pk_mul_f32 v[64:65], v[64:65], v[86:87]
	v_pk_add_f32 v[86:87], v[90:91], 1.0 op_sel_hi:[1,0]
	v_pk_mul_f32 v[64:65], v[64:65], v[130:131] op_sel_hi:[1,0]
	v_cvt_pk_bf16_f32 v63, v64, v65
	global_store_dwordx2 v[132:133], v[62:63], off offset:32
	v_rcp_f32_e32 v62, v87
	s_nop 0
	v_mul_f32_e32 v63, v71, v62
	v_mul_f32_e32 v64, 0xbfb8aa3b, v72
	v_mul_f32_e32 v65, 0xbfb8aa3b, v73
	v_exp_f32_e32 v64, v64
	v_exp_f32_e32 v65, v65
	v_rcp_f32_e32 v62, v86
	s_nop 0
	v_mul_f32_e32 v62, v70, v62
	v_pk_mul_f32 v[30:31], v[30:31], v[62:63]
	v_pk_add_f32 v[64:65], v[64:65], 1.0 op_sel_hi:[1,0]
	v_pk_mul_f32 v[30:31], v[30:31], v[130:131] op_sel_hi:[1,0]
	v_cvt_pk_bf16_f32 v30, v30, v31
	v_rcp_f32_e32 v31, v65
	s_nop 0
	v_mul_f32_e32 v63, v73, v31
	v_mul_f32_e32 v65, 0xbfb8aa3b, v42
	v_exp_f32_e32 v70, v65
	v_mul_f32_e32 v65, 0xbfb8aa3b, v43
	v_exp_f32_e32 v71, v65
	v_rcp_f32_e32 v31, v64
	s_nop 0
	v_mul_f32_e32 v62, v72, v31
	v_pk_mul_f32 v[32:33], v[32:33], v[62:63]
	v_pk_add_f32 v[62:63], v[70:71], 1.0 op_sel_hi:[1,0]
	v_pk_mul_f32 v[32:33], v[32:33], v[130:131] op_sel_hi:[1,0]
	v_cvt_pk_bf16_f32 v31, v32, v33
	global_store_dwordx2 v[132:133], v[30:31], off offset:64
	v_rcp_f32_e32 v30, v63
	s_nop 0
	v_mul_f32_e32 v31, v43, v30
	v_mul_f32_e32 v32, 0xbfb8aa3b, v44
	v_mul_f32_e32 v33, 0xbfb8aa3b, v45
	v_exp_f32_e32 v32, v32
	v_exp_f32_e32 v33, v33
	v_rcp_f32_e32 v30, v62
	s_nop 0
	v_mul_f32_e32 v30, v42, v30
	v_pk_mul_f32 v[10:11], v[10:11], v[30:31]
	v_pk_add_f32 v[32:33], v[32:33], 1.0 op_sel_hi:[1,0]
	v_pk_mul_f32 v[10:11], v[10:11], v[130:131] op_sel_hi:[1,0]
	v_cvt_pk_bf16_f32 v10, v10, v11
	v_rcp_f32_e32 v11, v33
	s_nop 0
	v_mul_f32_e32 v31, v45, v11
	v_rcp_f32_e32 v11, v32
	s_nop 0
	v_mul_f32_e32 v30, v44, v11
	v_pk_mul_f32 v[12:13], v[12:13], v[30:31]
	s_nop 0
	v_pk_mul_f32 v[12:13], v[12:13], v[130:131] op_sel_hi:[1,0]
	s_nop 0
	v_cvt_pk_bf16_f32 v11, v12, v13
	global_store_dwordx2 v[132:133], v[10:11], off offset:96
.LBB0_287:
	s_or_b64 exec, exec, s[48:49]
	v_or_b32_e32 v10, 16, v131
	v_add_u32_e32 v12, s50, v10
	v_cmp_gt_i32_e32 vcc, s65, v12
	s_and_b64 s[6:7], s[46:47], vcc
	s_and_saveexec_b64 s[46:47], s[6:7]
	s_cbranch_execz .LBB0_289
	s_add_i32 s99, s99, 4
	v_ashrrev_i32_e32 v13, 31, v12
	v_lshl_add_u64 v[10:11], v[12:13], 2, s[26:27]
	v_mul_f32_e32 v11, 0xbfb8aa3b, v74
	v_mul_f32_e32 v31, 0xbfb8aa3b, v75
	v_exp_f32_e32 v30, v11
	v_exp_f32_e32 v31, v31
	v_mul_f32_e32 v32, 0xbfb8aa3b, v76
	v_mul_f32_e32 v33, 0xbfb8aa3b, v77
	v_exp_f32_e32 v32, v32
	v_exp_f32_e32 v33, v33
	v_pk_add_f32 v[30:31], v[30:31], 1.0 op_sel_hi:[1,0]
	v_mul_f32_e32 v42, 0xbfb8aa3b, v46
	v_pk_add_f32 v[32:33], v[32:33], 1.0 op_sel_hi:[1,0]
	v_mul_f32_e32 v43, 0xbfb8aa3b, v47
	v_exp_f32_e32 v42, v42
	v_exp_f32_e32 v43, v43
	v_rcp_f32_e32 v11, v31
	s_nop 0
	v_mul_f32_e32 v31, v75, v11
	v_rcp_f32_e32 v11, v30
	s_nop 0
	v_mul_f32_e32 v30, v74, v11
	v_pk_add_f32 v[42:43], v[42:43], 1.0 op_sel_hi:[1,0]
	v_pk_mul_f32 v[30:31], v[54:55], v[30:31]
	v_rcp_f32_e32 v11, v33
	s_nop 0
	v_mul_f32_e32 v33, v77, v11
	v_add_u32_e32 v12, s63, v12
	v_rcp_f32_e32 v11, v32
	s_nop 0
	v_mul_f32_e32 v32, v76, v11
	v_ashrrev_i32_e32 v13, 31, v12
	v_lshlrev_b64 v[12:13], 9, v[12:13]
	v_pk_mul_f32 v[32:33], v[56:57], v[32:33]
	v_lshl_add_u64 v[12:13], s[20:21], 0, v[12:13]
	v_lshl_add_u64 v[12:13], v[12:13], 0, v[162:163]
	v_mov_b32_e32 v10, v245
	v_pk_mul_f32 v[30:31], v[30:31], v[10:11] op_sel_hi:[1,0]
	v_pk_mul_f32 v[32:33], v[32:33], v[10:11] op_sel_hi:[1,0]
	v_cvt_pk_bf16_f32 v30, v30, v31
	v_cvt_pk_bf16_f32 v31, v32, v33
	global_store_dwordx2 v[12:13], v[30:31], off
	v_rcp_f32_e32 v11, v43
	s_nop 0
	v_mul_f32_e32 v31, v47, v11
	v_mul_f32_e32 v30, 0xbfb8aa3b, v48
	v_exp_f32_e32 v32, v30
	v_mul_f32_e32 v30, 0xbfb8aa3b, v49
	v_exp_f32_e32 v33, v30
	v_rcp_f32_e32 v11, v42
	s_nop 0
	v_mul_f32_e32 v30, v46, v11
	v_pk_mul_f32 v[30:31], v[34:35], v[30:31]
	v_pk_add_f32 v[32:33], v[32:33], 1.0 op_sel_hi:[1,0]
	s_nop 0
	v_pk_mul_f32 v[30:31], v[30:31], v[10:11] op_sel_hi:[1,0]
	s_nop 0
	v_cvt_pk_bf16_f32 v30, v30, v31
	v_rcp_f32_e32 v11, v33
	s_nop 0
	v_mul_f32_e32 v33, v49, v11
	v_mul_f32_e32 v31, 0xbfb8aa3b, v18
	v_exp_f32_e32 v34, v31
	v_mul_f32_e32 v31, 0xbfb8aa3b, v19
	v_exp_f32_e32 v35, v31
	v_rcp_f32_e32 v11, v32
	s_nop 0
	v_mul_f32_e32 v32, v48, v11
	v_pk_mul_f32 v[32:33], v[36:37], v[32:33]
	v_pk_add_f32 v[34:35], v[34:35], 1.0 op_sel_hi:[1,0]
	s_nop 0
	v_pk_mul_f32 v[32:33], v[32:33], v[10:11] op_sel_hi:[1,0]
	s_nop 0
	v_cvt_pk_bf16_f32 v31, v32, v33
	global_store_dwordx2 v[12:13], v[30:31], off offset:32
	v_rcp_f32_e32 v11, v35
	s_nop 0
	v_mul_f32_e32 v19, v19, v11
	v_mul_f32_e32 v30, 0xbfb8aa3b, v20
	v_mul_f32_e32 v31, 0xbfb8aa3b, v21
	v_exp_f32_e32 v30, v30
	v_exp_f32_e32 v31, v31
	v_rcp_f32_e32 v11, v34
	s_nop 0
	v_mul_f32_e32 v18, v18, v11
	v_pk_mul_f32 v[14:15], v[14:15], v[18:19]
	v_pk_add_f32 v[30:31], v[30:31], 1.0 op_sel_hi:[1,0]
	s_nop 0
	v_pk_mul_f32 v[14:15], v[14:15], v[10:11] op_sel_hi:[1,0]
	s_nop 0
	v_cvt_pk_bf16_f32 v14, v14, v15
	v_rcp_f32_e32 v11, v31
	s_nop 0
	v_mul_f32_e32 v19, v21, v11
	v_mul_f32_e32 v15, 0xbfb8aa3b, v6
	v_exp_f32_e32 v32, v15
	v_mul_f32_e32 v15, 0xbfb8aa3b, v7
	v_exp_f32_e32 v33, v15
	v_rcp_f32_e32 v11, v30
	s_nop 0
	v_mul_f32_e32 v18, v20, v11
	v_pk_mul_f32 v[16:17], v[16:17], v[18:19]
	v_pk_add_f32 v[18:19], v[32:33], 1.0 op_sel_hi:[1,0]
	s_nop 0
	v_pk_mul_f32 v[16:17], v[16:17], v[10:11] op_sel_hi:[1,0]
	s_nop 0
	v_cvt_pk_bf16_f32 v15, v16, v17
	global_store_dwordx2 v[12:13], v[14:15], off offset:64
	v_rcp_f32_e32 v11, v19
	s_nop 0
	v_mul_f32_e32 v7, v7, v11
	v_mul_f32_e32 v14, 0xbfb8aa3b, v8
	v_mul_f32_e32 v15, 0xbfb8aa3b, v9
	v_exp_f32_e32 v14, v14
	v_exp_f32_e32 v15, v15
	v_rcp_f32_e32 v11, v18
	s_nop 0
	v_mul_f32_e32 v6, v6, v11
	v_pk_mul_f32 v[2:3], v[2:3], v[6:7]
	v_pk_add_f32 v[14:15], v[14:15], 1.0 op_sel_hi:[1,0]
	s_nop 0
	v_pk_mul_f32 v[2:3], v[2:3], v[10:11] op_sel_hi:[1,0]
	s_nop 0
	v_cvt_pk_bf16_f32 v2, v2, v3
	v_rcp_f32_e32 v3, v15
	s_nop 0
	v_mul_f32_e32 v7, v9, v3
	v_rcp_f32_e32 v3, v14
	s_nop 0
	v_mul_f32_e32 v6, v8, v3
	v_pk_mul_f32 v[4:5], v[4:5], v[6:7]
	s_nop 0
	v_pk_mul_f32 v[4:5], v[4:5], v[10:11] op_sel_hi:[1,0]
	s_nop 0
	v_cvt_pk_bf16_f32 v3, v4, v5
	global_store_dwordx2 v[12:13], v[2:3], off offset:96
.LBB0_289:
	s_or_b64 exec, exec, s[46:47]
	v_or_b32_e32 v2, 32, v131
	v_add_u32_e32 v4, s50, v2
	v_cmp_gt_i32_e32 vcc, s65, v4
	s_and_b64 s[6:7], s[44:45], vcc
	s_and_saveexec_b64 s[44:45], s[6:7]
	s_cbranch_execz .LBB0_291
	s_add_i32 s99, s99, 4
	v_ashrrev_i32_e32 v5, 31, v4
	v_lshl_add_u64 v[2:3], v[4:5], 2, s[26:27]
	v_mul_f32_e32 v3, 0xbfb8aa3b, v78
	v_mul_f32_e32 v7, 0xbfb8aa3b, v79
	v_exp_f32_e32 v6, v3
	v_exp_f32_e32 v7, v7
	v_mul_f32_e32 v8, 0xbfb8aa3b, v80
	v_mul_f32_e32 v9, 0xbfb8aa3b, v81
	v_exp_f32_e32 v8, v8
	v_exp_f32_e32 v9, v9
	v_pk_add_f32 v[6:7], v[6:7], 1.0 op_sel_hi:[1,0]
	v_mul_f32_e32 v10, 0xbfb8aa3b, v58
	v_pk_add_f32 v[8:9], v[8:9], 1.0 op_sel_hi:[1,0]
	v_mul_f32_e32 v11, 0xbfb8aa3b, v59
	v_exp_f32_e32 v10, v10
	v_exp_f32_e32 v11, v11
	v_rcp_f32_e32 v3, v7
	s_nop 0
	v_mul_f32_e32 v7, v79, v3
	v_rcp_f32_e32 v3, v6
	s_nop 0
	v_mul_f32_e32 v6, v78, v3
	v_pk_add_f32 v[10:11], v[10:11], 1.0 op_sel_hi:[1,0]
	v_pk_mul_f32 v[6:7], v[82:83], v[6:7]
	v_rcp_f32_e32 v3, v9
	s_nop 0
	v_mul_f32_e32 v9, v81, v3
	v_add_u32_e32 v4, s63, v4
	v_rcp_f32_e32 v3, v8
	s_nop 0
	v_mul_f32_e32 v8, v80, v3
	v_ashrrev_i32_e32 v5, 31, v4
	v_lshlrev_b64 v[4:5], 9, v[4:5]
	v_pk_mul_f32 v[8:9], v[84:85], v[8:9]
	v_lshl_add_u64 v[4:5], s[20:21], 0, v[4:5]
	v_lshl_add_u64 v[4:5], v[4:5], 0, v[162:163]
	v_mov_b32_e32 v2, v246
	v_pk_mul_f32 v[6:7], v[6:7], v[2:3] op_sel_hi:[1,0]
	v_pk_mul_f32 v[8:9], v[8:9], v[2:3] op_sel_hi:[1,0]
	v_cvt_pk_bf16_f32 v6, v6, v7
	v_cvt_pk_bf16_f32 v7, v8, v9
	global_store_dwordx2 v[4:5], v[6:7], off
	v_rcp_f32_e32 v3, v11
	s_nop 0
	v_mul_f32_e32 v7, v59, v3
	v_mul_f32_e32 v6, 0xbfb8aa3b, v60
	v_exp_f32_e32 v8, v6
	v_mul_f32_e32 v6, 0xbfb8aa3b, v61
	v_exp_f32_e32 v9, v6
	v_rcp_f32_e32 v3, v10
	s_nop 0
	v_mul_f32_e32 v6, v58, v3
	v_pk_mul_f32 v[6:7], v[66:67], v[6:7]
	v_pk_add_f32 v[8:9], v[8:9], 1.0 op_sel_hi:[1,0]
	s_nop 0
	v_pk_mul_f32 v[6:7], v[6:7], v[2:3] op_sel_hi:[1,0]
	s_nop 0
	v_cvt_pk_bf16_f32 v6, v6, v7
	v_rcp_f32_e32 v3, v9
	s_nop 0
	v_mul_f32_e32 v9, v61, v3
	v_mul_f32_e32 v7, 0xbfb8aa3b, v38
	v_exp_f32_e32 v10, v7
	v_mul_f32_e32 v7, 0xbfb8aa3b, v39
	v_exp_f32_e32 v11, v7
	v_rcp_f32_e32 v3, v8
	s_nop 0
	v_mul_f32_e32 v8, v60, v3
	v_pk_mul_f32 v[8:9], v[68:69], v[8:9]
	v_pk_add_f32 v[10:11], v[10:11], 1.0 op_sel_hi:[1,0]
	s_nop 0
	v_pk_mul_f32 v[8:9], v[8:9], v[2:3] op_sel_hi:[1,0]
	s_nop 0
	v_cvt_pk_bf16_f32 v7, v8, v9
	global_store_dwordx2 v[4:5], v[6:7], off offset:32
	v_rcp_f32_e32 v3, v11
	s_nop 0
	v_mul_f32_e32 v7, v39, v3
	v_mul_f32_e32 v6, 0xbfb8aa3b, v40
	v_exp_f32_e32 v8, v6
	v_mul_f32_e32 v6, 0xbfb8aa3b, v41
	v_exp_f32_e32 v9, v6
	v_rcp_f32_e32 v3, v10
	s_nop 0
	v_mul_f32_e32 v6, v38, v3
	v_pk_mul_f32 v[6:7], v[50:51], v[6:7]
	v_pk_add_f32 v[8:9], v[8:9], 1.0 op_sel_hi:[1,0]
	s_nop 0
	v_pk_mul_f32 v[6:7], v[6:7], v[2:3] op_sel_hi:[1,0]
	s_nop 0
	v_cvt_pk_bf16_f32 v6, v6, v7
	v_rcp_f32_e32 v3, v9
	s_nop 0
	v_mul_f32_e32 v9, v41, v3
	v_mul_f32_e32 v7, 0xbfb8aa3b, v22
	v_exp_f32_e32 v10, v7
	v_mul_f32_e32 v7, 0xbfb8aa3b, v23
	v_exp_f32_e32 v11, v7
	v_rcp_f32_e32 v3, v8
	s_nop 0
	v_mul_f32_e32 v8, v40, v3
	v_pk_mul_f32 v[8:9], v[52:53], v[8:9]
	v_pk_add_f32 v[10:11], v[10:11], 1.0 op_sel_hi:[1,0]
	s_nop 0
	v_pk_mul_f32 v[8:9], v[8:9], v[2:3] op_sel_hi:[1,0]
	s_nop 0
	v_cvt_pk_bf16_f32 v7, v8, v9
	global_store_dwordx2 v[4:5], v[6:7], off offset:64
	v_rcp_f32_e32 v3, v11
	s_nop 0
	v_mul_f32_e32 v7, v23, v3
	v_mul_f32_e32 v6, 0xbfb8aa3b, v24
	v_exp_f32_e32 v8, v6
	v_mul_f32_e32 v6, 0xbfb8aa3b, v25
	v_exp_f32_e32 v9, v6
	v_rcp_f32_e32 v3, v10
	s_nop 0
	v_mul_f32_e32 v6, v22, v3
	v_pk_mul_f32 v[6:7], v[26:27], v[6:7]
	v_pk_add_f32 v[8:9], v[8:9], 1.0 op_sel_hi:[1,0]
	s_nop 0
	v_pk_mul_f32 v[6:7], v[6:7], v[2:3] op_sel_hi:[1,0]
	s_nop 0
	v_cvt_pk_bf16_f32 v6, v6, v7
	v_rcp_f32_e32 v3, v9
	s_nop 0
	v_mul_f32_e32 v9, v25, v3
	v_rcp_f32_e32 v3, v8
	s_nop 0
	v_mul_f32_e32 v8, v24, v3
	v_pk_mul_f32 v[8:9], v[28:29], v[8:9]
	s_nop 0
	v_pk_mul_f32 v[2:3], v[8:9], v[2:3] op_sel_hi:[1,0]
	s_nop 0
	v_cvt_pk_bf16_f32 v7, v2, v3
	global_store_dwordx2 v[4:5], v[6:7], off offset:96
.LBB0_291:
	s_or_b64 exec, exec, s[44:45]
	v_or_b32_e32 v2, 48, v131
	v_add_u32_e32 v4, s50, v2
	v_cmp_gt_i32_e32 vcc, s65, v4
	s_and_b64 s[6:7], s[42:43], vcc
	s_and_saveexec_b64 s[42:43], s[6:7]
	s_cbranch_execz .LBB0_262
	s_add_i32 s99, s99, 4
	v_ashrrev_i32_e32 v5, 31, v4
	v_lshl_add_u64 v[2:3], v[4:5], 2, s[26:27]
	v_mul_f32_e32 v3, 0xbfb8aa3b, v122
	v_mul_f32_e32 v7, 0xbfb8aa3b, v123
	v_exp_f32_e32 v6, v3
	v_exp_f32_e32 v7, v7
	v_mul_f32_e32 v8, 0xbfb8aa3b, v124
	v_mul_f32_e32 v9, 0xbfb8aa3b, v125
	v_exp_f32_e32 v8, v8
	v_exp_f32_e32 v9, v9
	v_pk_add_f32 v[6:7], v[6:7], 1.0 op_sel_hi:[1,0]
	v_mul_f32_e32 v10, 0xbfb8aa3b, v114
	v_pk_add_f32 v[8:9], v[8:9], 1.0 op_sel_hi:[1,0]
	v_mul_f32_e32 v11, 0xbfb8aa3b, v115
	v_exp_f32_e32 v10, v10
	v_exp_f32_e32 v11, v11
	v_rcp_f32_e32 v3, v7
	s_nop 0
	v_mul_f32_e32 v7, v123, v3
	v_rcp_f32_e32 v3, v6
	s_nop 0
	v_mul_f32_e32 v6, v122, v3
	v_pk_add_f32 v[10:11], v[10:11], 1.0 op_sel_hi:[1,0]
	v_pk_mul_f32 v[6:7], v[126:127], v[6:7]
	v_rcp_f32_e32 v3, v9
	s_nop 0
	v_mul_f32_e32 v9, v125, v3
	v_add_u32_e32 v4, s63, v4
	v_rcp_f32_e32 v3, v8
	s_nop 0
	v_mul_f32_e32 v8, v124, v3
	v_ashrrev_i32_e32 v5, 31, v4
	v_lshlrev_b64 v[4:5], 9, v[4:5]
	v_pk_mul_f32 v[8:9], v[128:129], v[8:9]
	v_lshl_add_u64 v[4:5], s[20:21], 0, v[4:5]
	v_lshl_add_u64 v[4:5], v[4:5], 0, v[162:163]
	v_mov_b32_e32 v2, v247
	v_pk_mul_f32 v[6:7], v[6:7], v[2:3] op_sel_hi:[1,0]
	v_pk_mul_f32 v[8:9], v[8:9], v[2:3] op_sel_hi:[1,0]
	v_cvt_pk_bf16_f32 v6, v6, v7
	v_cvt_pk_bf16_f32 v7, v8, v9
	global_store_dwordx2 v[4:5], v[6:7], off
	v_rcp_f32_e32 v3, v11
	s_nop 0
	v_mul_f32_e32 v7, v115, v3
	v_mul_f32_e32 v6, 0xbfb8aa3b, v116
	v_exp_f32_e32 v8, v6
	v_mul_f32_e32 v6, 0xbfb8aa3b, v117
	v_exp_f32_e32 v9, v6
	v_rcp_f32_e32 v3, v10
	s_nop 0
	v_mul_f32_e32 v6, v114, v3
	v_pk_mul_f32 v[6:7], v[118:119], v[6:7]
	v_pk_add_f32 v[8:9], v[8:9], 1.0 op_sel_hi:[1,0]
	s_nop 0
	v_pk_mul_f32 v[6:7], v[6:7], v[2:3] op_sel_hi:[1,0]
	s_nop 0
	v_cvt_pk_bf16_f32 v6, v6, v7
	v_rcp_f32_e32 v3, v9
	s_nop 0
	v_mul_f32_e32 v9, v117, v3
	v_mul_f32_e32 v7, 0xbfb8aa3b, v106
	v_exp_f32_e32 v10, v7
	v_mul_f32_e32 v7, 0xbfb8aa3b, v107
	v_exp_f32_e32 v11, v7
	v_rcp_f32_e32 v3, v8
	s_nop 0
	v_mul_f32_e32 v8, v116, v3
	v_pk_mul_f32 v[8:9], v[120:121], v[8:9]
	v_pk_add_f32 v[10:11], v[10:11], 1.0 op_sel_hi:[1,0]
	s_nop 0
	v_pk_mul_f32 v[8:9], v[8:9], v[2:3] op_sel_hi:[1,0]
	s_nop 0
	v_cvt_pk_bf16_f32 v7, v8, v9
	global_store_dwordx2 v[4:5], v[6:7], off offset:32
	v_rcp_f32_e32 v3, v11
	s_nop 0
	v_mul_f32_e32 v7, v107, v3
	v_mul_f32_e32 v6, 0xbfb8aa3b, v108
	v_exp_f32_e32 v8, v6
	v_mul_f32_e32 v6, 0xbfb8aa3b, v109
	v_exp_f32_e32 v9, v6
	v_rcp_f32_e32 v3, v10
	s_nop 0
	v_mul_f32_e32 v6, v106, v3
	v_pk_mul_f32 v[6:7], v[110:111], v[6:7]
	v_pk_add_f32 v[8:9], v[8:9], 1.0 op_sel_hi:[1,0]
	s_nop 0
	v_pk_mul_f32 v[6:7], v[6:7], v[2:3] op_sel_hi:[1,0]
	s_nop 0
	v_cvt_pk_bf16_f32 v6, v6, v7
	v_rcp_f32_e32 v3, v9
	s_nop 0
	v_mul_f32_e32 v9, v109, v3
	v_mul_f32_e32 v7, 0xbfb8aa3b, v102
	v_exp_f32_e32 v10, v7
	v_mul_f32_e32 v7, 0xbfb8aa3b, v103
	v_exp_f32_e32 v11, v7
	v_rcp_f32_e32 v3, v8
	s_nop 0
	v_mul_f32_e32 v8, v108, v3
	v_pk_mul_f32 v[8:9], v[112:113], v[8:9]
	v_pk_add_f32 v[10:11], v[10:11], 1.0 op_sel_hi:[1,0]
	s_nop 0
	v_pk_mul_f32 v[8:9], v[8:9], v[2:3] op_sel_hi:[1,0]
	s_nop 0
	v_cvt_pk_bf16_f32 v7, v8, v9
	global_store_dwordx2 v[4:5], v[6:7], off offset:64
	v_rcp_f32_e32 v3, v11
	s_nop 0
	v_mul_f32_e32 v7, v103, v3
	v_mul_f32_e32 v6, 0xbfb8aa3b, v104
	v_exp_f32_e32 v8, v6
	v_mul_f32_e32 v6, 0xbfb8aa3b, v105
	v_exp_f32_e32 v9, v6
	v_rcp_f32_e32 v3, v10
	s_nop 0
	v_mul_f32_e32 v6, v102, v3
	v_pk_mul_f32 v[6:7], v[98:99], v[6:7]
	v_pk_add_f32 v[8:9], v[8:9], 1.0 op_sel_hi:[1,0]
	s_nop 0
	v_pk_mul_f32 v[6:7], v[6:7], v[2:3] op_sel_hi:[1,0]
	s_nop 0
	v_cvt_pk_bf16_f32 v6, v6, v7
	v_rcp_f32_e32 v3, v9
	s_nop 0
	v_mul_f32_e32 v9, v105, v3
	v_rcp_f32_e32 v3, v8
	s_nop 0
	v_mul_f32_e32 v8, v104, v3
	v_pk_mul_f32 v[8:9], v[100:101], v[8:9]
	s_nop 0
	v_pk_mul_f32 v[2:3], v[8:9], v[2:3] op_sel_hi:[1,0]
	s_nop 0
	v_cvt_pk_bf16_f32 v7, v2, v3
	global_store_dwordx2 v[4:5], v[6:7], off offset:96
	s_branch .LBB0_262

.LBB0_864:
	v_readlane_b32 s7, v254, 0
	s_lshr_b32 s5, s7, 2
	s_and_b32 s4, s7, 7
	s_and_b32 s5, s5, 0x3ffffff8
	s_or_b32 s4, s5, s4
	s_sub_i32 s5, 63, s4
	s_lshl_b32 s4, s4, 2
	s_add_i32 s4, s4, 0
	s_add_i32 s6, s4, 0x21400
	v_mov_b32_e32 v2, s6
	s_waitcnt lgkmcnt(0)
	s_barrier
	ds_read_b32 v2, v2
	s_lshl_b32 s5, s5, 2
	s_add_i32 s5, s5, 0
	s_add_i32 s4, s4, 0x21600
	s_add_i32 s6, s5, 0x21500
	v_mov_b32_e32 v4, s4
	s_add_i32 s4, s5, 0x21700
	v_mov_b32_e32 v3, s6
	v_mov_b32_e32 v5, s4
	ds_read_b32 v3, v3
	ds_read_b32 v4, v4
	ds_read_b32 v5, v5
	s_waitcnt lgkmcnt(3)
	v_readfirstlane_b32 s33, v2
	s_lshl_b32 s4, s33, 2
	s_add_i32 s5, 0, 0x21000
	s_add_i32 s4, s5, s4
	s_waitcnt lgkmcnt(2)
	v_readfirstlane_b32 s52, v3
	v_mov_b32_e32 v2, s4
	s_lshl_b32 s4, s52, 2
	s_add_i32 s4, s5, s4
	s_waitcnt lgkmcnt(1)
	v_readfirstlane_b32 s53, v4
	v_mov_b32_e32 v3, s4
	s_lshl_b32 s4, s53, 2
	s_add_i32 s4, s5, s4
	s_waitcnt lgkmcnt(0)
	v_readfirstlane_b32 s54, v5
	v_mov_b32_e32 v4, s4
	s_lshl_b32 s4, s54, 2
	s_add_i32 s4, s5, s4
	v_mov_b32_e32 v5, s4
	ds_read_b32 v2, v2
	ds_read_b32 v3, v3
	ds_read_b32 v4, v4
	ds_read_b32 v5, v5
	s_waitcnt lgkmcnt(0)
	s_barrier
	s_load_dwordx4 s[16:19], s[0:1], 0x120
	s_load_dwordx2 s[10:11], s[0:1], 0x140
	s_bfe_u32 s12, s7, 0x20003
	s_bitcmp0_b32 s7, 5
	s_load_dwordx2 s[6:7], s[0:1], 0x58
	s_load_dwordx2 s[8:9], s[0:1], 0xe8
	s_cselect_b64 s[4:5], -1, 0
	s_lshl_b32 s13, s12, 8
	s_add_i32 s14, s13, 0x300
	s_lshl_b32 s12, s12, 7
	s_waitcnt lgkmcnt(0)
	s_add_u32 s20, s10, s12
	s_mov_b32 s55, 0
	v_readfirstlane_b32 s56, v2
	v_readfirstlane_b32 s57, v3
	v_readfirstlane_b32 s58, v4
	v_readfirstlane_b32 s59, v5
	s_addc_u32 s21, s11, 0
	v_mov_b32_e32 v163, 0
	s_movk_i32 s60, 0xf800
	v_mov_b32_e32 v166, s14
	v_mov_b32_e32 v167, s13
	s_add_i32 s61, 0, 0x20000
	v_lshlrev_b32_e64 v244, 2, s33
	v_lshlrev_b32_e64 v245, 2, s52
	v_lshlrev_b32_e64 v246, 2, s53
	v_lshlrev_b32_e64 v247, 2, s54
	global_load_dword v244, v244, s[2:3] offset:1024
	global_load_dword v245, v245, s[2:3] offset:1024
	global_load_dword v246, v246, s[2:3] offset:1024
	global_load_dword v247, v247, s[2:3] offset:1024
	s_waitcnt vmcnt(0)
	v_readfirstlane_b32 s98, v244
	v_readfirstlane_b32 s99, v245
	v_readfirstlane_b32 s100, v246
	v_readfirstlane_b32 s101, v247
	s_nop 3
	v_writelane_b32 v253, s98, 0
	v_writelane_b32 v253, s99, 1
	v_writelane_b32 v253, s100, 2
	v_writelane_b32 v253, s101, 3
	v_writelane_b32 v253, s33, 4
	v_writelane_b32 v253, s52, 5
	v_writelane_b32 v253, s53, 6
	v_writelane_b32 v253, s54, 7
	s_nop 1
	s_mov_b32 s98, 0
	s_mov_b32 s99, -1
	v_readfirstlane_b32 s100, v0
	s_lshl_b32 s100, s100, 8
	s_and_b32 s100, s100, 0xffffc000
	s_add_i32 s67, s100, 0
	v_and_b32_e32 v240, 31, v0
	v_cmp_gt_u32_e32 vcc, 16, v240
	v_ashrrev_i32_e32 v243, 5, v0
	v_cndmask_b32_e32 v231, v166, v167, vcc
	v_lshl_add_u32 v241, v240, 4, v231
	v_lshl_or_b32 v168, v243, 13, v241

.Lmy_iss_bp:
	s_sub_i32 s100, 3, s99
	s_and_b64 vcc, s[4:5], exec
	s_cselect_b32 s100, s99, s100
	s_nop 3
	v_readlane_b32 s101, v253, s100
	s_add_i32 s100, s100, 4
	s_nop 3
	v_readlane_b32 s100, v253, s100
	s_sub_i32 s101, s101, s98
	s_min_i32 s101, s101, 0x200
	v_mov_b32_e32 v228, s98
	s_add_i32 s99, s101, 0x7f
	s_lshr_b32 s99, s99, 7
	s_add_i32 s101, s101, s98
	v_readfirstlane_b32 vcc_lo, v0
	s_ashr_i32 vcc_lo, vcc_lo, 2
	s_and_b32 vcc_lo, vcc_lo, -16
	s_mul_i32 vcc_lo, vcc_lo, s99
	s_add_i32 vcc_lo, vcc_lo, s98
	v_bfe_u32 v229, v0, 3, 3
	v_or_b32_e32 v229, vcc_lo, v229
	v_add_u32_e32 v232, 0, v229
	v_cmp_gt_i32_e32 vcc, s101, v232
	v_cndmask_b32_e32 v232, v228, v232, vcc
	v_lshlrev_b32_e32 v232, 2, v232
	v_add_u32_e32 v233, 8, v229
	v_cmp_gt_i32_e32 vcc, s101, v233
	v_cndmask_b32_e32 v233, v228, v233, vcc
	v_lshlrev_b32_e32 v233, 2, v233
	v_add_u32_e32 v234, 16, v229
	v_cmp_gt_i32_e32 vcc, s101, v234
	v_cndmask_b32_e32 v234, v228, v234, vcc
	v_lshlrev_b32_e32 v234, 2, v234
	v_add_u32_e32 v235, 24, v229
	v_cmp_gt_i32_e32 vcc, s101, v235
	v_cndmask_b32_e32 v235, v228, v235, vcc
	v_lshlrev_b32_e32 v235, 2, v235
	v_add_u32_e32 v236, 32, v229
	v_cmp_gt_i32_e32 vcc, s101, v236
	v_cndmask_b32_e32 v236, v228, v236, vcc
	v_lshlrev_b32_e32 v236, 2, v236
	v_add_u32_e32 v237, 40, v229
	v_cmp_gt_i32_e32 vcc, s101, v237
	v_cndmask_b32_e32 v237, v228, v237, vcc
	v_lshlrev_b32_e32 v237, 2, v237
	v_add_u32_e32 v238, 48, v229
	v_cmp_gt_i32_e32 vcc, s101, v238
	v_cndmask_b32_e32 v238, v228, v238, vcc
	v_lshlrev_b32_e32 v238, 2, v238
	v_add_u32_e32 v239, 56, v229
	v_cmp_gt_i32_e32 vcc, s101, v239
	v_cndmask_b32_e32 v239, v228, v239, vcc
	v_lshlrev_b32_e32 v239, 2, v239
	s_lshl_b32 s99, s100, 16
	s_add_u32 s98, s16, s99
	s_addc_u32 s99, s17, 0
	global_load_dword v232, v232, s[98:99]
	global_load_dword v233, v233, s[98:99]
	global_load_dword v234, v234, s[98:99]
	global_load_dword v235, v235, s[98:99]
	global_load_dword v236, v236, s[98:99]
	global_load_dword v237, v237, s[98:99]
	global_load_dword v238, v238, s[98:99]
	global_load_dword v239, v239, s[98:99]
	s_lshl_b32 s99, s100, 21
	s_add_u32 s98, s6, s99
	s_addc_u32 s99, s7, 0
	s_add_u32 s98, s98, 0x20000000
	s_addc_u32 s99, s99, 0
	v_add_u32_e32 v230, 0x800, v168
	s_mov_b32 s100, m0
	s_add_i32 m0, s67, 0x2000
	s_nop 0
	global_load_lds_dwordx4 v168, s[98:99]
	s_add_i32 m0, s67, 0x2400
	s_nop 0
	global_load_lds_dwordx4 v230, s[98:99]
	s_add_u32 s98, s98, 0x1000
	s_addc_u32 s99, s99, 0
	s_add_i32 m0, s67, 0x2800
	s_nop 0
	global_load_lds_dwordx4 v168, s[98:99]
	s_add_i32 m0, s67, 0x2c00
	s_nop 0
	global_load_lds_dwordx4 v230, s[98:99]
	s_add_u32 s98, s98, 0x1f000
	s_addc_u32 s99, s99, 0
	s_add_i32 m0, s67, 0x3000
	s_nop 0
	global_load_lds_dwordx4 v168, s[98:99]
	s_add_i32 m0, s67, 0x3400
	s_nop 0
	global_load_lds_dwordx4 v230, s[98:99]
	s_add_u32 s98, s98, 0x1000
	s_addc_u32 s99, s99, 0
	s_add_i32 m0, s67, 0x3800
	s_nop 0
	global_load_lds_dwordx4 v168, s[98:99]
	s_add_i32 m0, s67, 0x3c00
	s_nop 0
	global_load_lds_dwordx4 v230, s[98:99]
	s_mov_b32 m0, s100

.LBB0_866:
	s_sub_i32 s12, 3, s55
	s_and_b64 s[10:11], s[4:5], exec
	s_cselect_b32 s22, s55, s12
	s_nop 3
	v_readlane_b32 s62, v253, s22
	s_cmp_eq_u32 s22, 2
	s_cselect_b64 s[12:13], -1, 0
	s_and_b64 s[10:11], s[12:13], exec
	s_cselect_b32 s23, s53, s54
	s_cmp_eq_u32 s22, 1
	s_cselect_b64 s[14:15], -1, 0
	s_and_b64 s[10:11], s[14:15], exec
	s_cselect_b32 s24, s52, s23
	s_cmp_eq_u32 s22, 0
	s_cselect_b64 s[22:23], -1, 0
	s_and_b64 s[10:11], s[22:23], exec
	s_cselect_b32 s10, s33, s24
	s_ashr_i32 s11, s10, 31
	s_cmp_lt_i32 s62, 1
	s_cbranch_scc1 .LBB0_865
	s_and_b64 s[12:13], s[12:13], exec
	s_cselect_b32 s24, s58, s59
	s_and_b64 s[12:13], s[14:15], exec
	s_cselect_b32 s14, s57, s24
	s_and_b64 s[12:13], s[22:23], exec
	s_cselect_b32 s63, s56, s14
	s_lshl_b64 s[12:13], s[10:11], 21
	s_add_u32 s12, s6, s12
	s_addc_u32 s13, s7, s13
	s_add_u32 s22, s12, 0x20000000
	s_addc_u32 s23, s13, 0
	s_lshl_b64 s[10:11], s[10:11], 16
	s_add_u32 s24, s16, s10
	s_addc_u32 s25, s17, s11
	s_add_u32 s26, s18, s10
	s_addc_u32 s27, s19, s11
	s_add_u32 s28, s12, 0x20001000
	s_addc_u32 s29, s13, 0
	s_add_u32 s30, s12, 0x20020000
	s_addc_u32 s31, s13, 0
	s_add_u32 s34, s12, 0x20021000
	s_addc_u32 s35, s13, 0
	s_add_u32 s36, s12, 0x20040000
	s_addc_u32 s37, s13, 0
	s_add_u32 s38, s12, 0x20041000
	s_addc_u32 s39, s13, 0
	s_mov_b32 s64, 0
	s_branch .LBB0_869

.LBB0_869:
	s_sub_i32 s11, s62, s64
	v_mov_b32_e32 v162, v0
	s_min_i32 s11, s11, 0x200
	s_add_i32 s12, s11, 0x7f
	v_readfirstlane_b32 s10, v162
	s_lshr_b32 s66, s12, 7
	s_ashr_i32 s12, s10, 2
	s_and_b32 s12, s12, -16
	s_mul_i32 s12, s12, s66
	s_add_i32 s12, s12, s64
	v_bfe_u32 v2, v162, 3, 3
	v_or_b32_e32 v10, s12, v2
	s_add_i32 s65, s11, s64
	v_mov_b32_e32 v11, s64
	v_cmp_gt_i32_e32 vcc, s65, v10
	v_or_b32_e32 v4, 8, v10
	v_add_u32_e32 v6, 16, v10
	v_cndmask_b32_e32 v2, v11, v10, vcc
	v_cmp_gt_i32_e32 vcc, s65, v4
	s_cmpk_gt_u32 s11, 0x80
	s_cselect_b64 s[44:45], -1, 0
	v_cndmask_b32_e32 v4, v11, v4, vcc
	v_cmp_gt_i32_e32 vcc, s65, v6
	s_and_b64 vcc, s[44:45], vcc
	v_add_u32_e32 v8, 24, v10
	v_cndmask_b32_e32 v6, v11, v6, vcc
	v_cmp_gt_i32_e32 vcc, s65, v8
	s_and_b64 vcc, s[44:45], vcc
	v_ashrrev_i32_e32 v3, 31, v2
	v_ashrrev_i32_e32 v7, 31, v6
	v_cndmask_b32_e32 v8, v11, v8, vcc
	v_lshl_add_u64 v[2:3], v[2:3], 2, s[24:25]
	v_ashrrev_i32_e32 v5, 31, v4
	v_lshl_add_u64 v[6:7], v[6:7], 2, s[24:25]
	v_ashrrev_i32_e32 v9, 31, v8
	v_lshl_add_u64 v[4:5], v[4:5], 2, s[24:25]
	v_lshl_add_u64 v[8:9], v[8:9], 2, s[24:25]
	s_cmp_lt_u32 s99, 16
	s_cbranch_scc1 .Lmy_w16_b
	s_waitcnt vmcnt(16)
	s_branch .Lmy_wd_b

.Lmy_wd_b:
	v_mov_b32_e32 v12, v232
	v_mov_b32_e32 v13, v233
	s_nop 0
	v_mov_b32_e32 v6, v234
	s_nop 0
	v_mov_b32_e32 v7, v235
	v_add_u32_e32 v2, 32, v10
	s_cmpk_gt_u32 s11, 0x100
	s_cselect_b64 s[42:43], -1, 0
	v_cmp_gt_i32_e32 vcc, s65, v2
	s_and_b64 vcc, s[42:43], vcc
	v_add_u32_e32 v4, 40, v10
	v_cndmask_b32_e32 v2, v11, v2, vcc
	v_cmp_gt_i32_e32 vcc, s65, v4
	s_and_b64 vcc, s[42:43], vcc
	v_ashrrev_i32_e32 v3, 31, v2
	v_cndmask_b32_e32 v4, v11, v4, vcc
	v_lshl_add_u64 v[2:3], v[2:3], 2, s[24:25]
	v_ashrrev_i32_e32 v5, 31, v4
	v_lshl_add_u64 v[4:5], v[4:5], 2, s[24:25]
	v_mov_b32_e32 v8, v236
	v_mov_b32_e32 v9, v237
	v_add_u32_e32 v2, 48, v10
	s_cmpk_gt_u32 s11, 0x180
	s_cselect_b64 s[40:41], -1, 0
	v_cmp_gt_i32_e32 vcc, s65, v2
	s_and_b64 vcc, s[40:41], vcc
	v_add_u32_e32 v4, 56, v10
	v_cndmask_b32_e32 v2, v11, v2, vcc
	v_cmp_gt_i32_e32 vcc, s65, v4
	s_and_b64 vcc, s[40:41], vcc
	v_ashrrev_i32_e32 v3, 31, v2
	v_cndmask_b32_e32 v4, v11, v4, vcc
	v_lshl_add_u64 v[2:3], v[2:3], 2, s[24:25]
	v_ashrrev_i32_e32 v5, 31, v4
	v_lshl_add_u64 v[4:5], v[4:5], 2, s[24:25]
	v_mov_b32_e32 v131, v238
	v_mov_b32_e32 v130, v239
	v_and_b32_e32 v10, 31, v162
	v_and_b32_e32 v2, 7, v162
	v_bfe_u32 v3, v162, 4, 2
	v_cmp_gt_u32_e32 vcc, 16, v10
	v_bitop3_b32 v2, v3, v2, 4 bitop3:0x36
	v_ashrrev_i32_e32 v11, 5, v162
	v_cndmask_b32_e32 v15, v166, v167, vcc
	v_bitop3_b32 v14, v3, v162, 7 bitop3:0x78
	v_lshlrev_b32_e32 v132, 4, v2
	v_lshl_add_u32 v2, v10, 4, v15
	v_lshlrev_b32_e32 v133, 4, v14
	v_lshl_or_b32 v168, v11, 13, v2
	v_readfirstlane_b32 s98, v162
	s_ashr_i32 s98, s98, 6
	s_mul_i32 s98, s66, s98
	s_lshl_b32 s98, s98, 4
	v_and_or_b32 v252, v162, 15, s64
	v_add_u32_e32 v252, s98, v252
	v_lshlrev_b32_e32 v252, 2, v252
	global_load_dword v244, v252, s[26:27]
	global_load_dword v245, v252, s[26:27] offset:64
	global_load_dword v246, v252, s[26:27] offset:128
	global_load_dword v247, v252, s[26:27] offset:192
	v_lshrrev_b32_e32 v5, 4, v162
	v_lshlrev_b32_e32 v3, 11, v3
	s_lshl_b32 s10, s10, 8
	s_and_b32 s10, s10, 0xffffc000
	v_and_b32_e32 v4, 15, v162
	s_add_i32 s67, s10, 0
	s_add_i32 s68, s67, 0x400
	v_and_b32_e32 v248, 63, v162
	v_lshlrev_b32_e32 v248, 4, v248
	v_add_u32_e32 v248, s67, v248
	s_mov_b64 s[10:11], -1
	s_mov_b64 s[12:13], 0
	s_cmp_lt_i32 s66, 2
	s_mov_b64 s[14:15], 0
	s_waitcnt vmcnt(19)
	v_lshlrev_b32_e32 v2, 8, v12
	v_and_or_b32 v169, v2, s60, v133
	s_waitcnt vmcnt(18)
	v_lshlrev_b32_e32 v2, 8, v13
	v_and_or_b32 v170, v2, s60, v132
	s_waitcnt vmcnt(17)
	v_lshlrev_b32_e32 v2, 8, v6
	s_waitcnt vmcnt(16)
	v_lshlrev_b32_e32 v6, 8, v7
	v_and_or_b32 v175, v6, s60, v132
	v_and_or_b32 v174, v2, s60, v133
	s_waitcnt vmcnt(15)
	v_lshlrev_b32_e32 v2, 8, v8
	s_waitcnt vmcnt(14)
	v_lshlrev_b32_e32 v6, 8, v9
	v_and_or_b32 v177, v6, s60, v132
	v_lshlrev_b32_e32 v6, 3, v162
	v_and_or_b32 v176, v2, s60, v133
	v_lshlrev_b32_e32 v2, 10, v11
	v_and_b32_e32 v6, 24, v6
	v_add3_u32 v173, s61, v2, v6
	v_bfe_u32 v2, v162, 2, 3
	v_bitop3_b32 v134, v2, v5, 4 bitop3:0x78
	v_bfe_u32 v2, v162, 2, 2
	v_lshlrev_b32_e32 v7, 8, v2
	v_add3_u32 v3, s61, v3, v7
	v_lshrrev_b32_e32 v7, 2, v162
	v_and_or_b32 v2, v7, 4, v2
	v_lshlrev_b32_e32 v2, 5, v2
	v_add3_u32 v171, v3, v6, v2
	v_bfe_u32 v3, v162, 1, 3
	v_bitop3_b32 v3, v5, v3, 3 bitop3:0x6c
	v_lshlrev_b32_e32 v2, 7, v4
	v_lshlrev_b32_e32 v3, 4, v3
	v_add3_u32 v172, s67, v2, v3
	s_cbranch_scc1 .LBB0_881
	s_cmp_gt_i32 s66, 2
	s_cbranch_scc0 .LBB0_875
	s_cmp_eq_u32 s66, 3
	s_mov_b64 s[14:15], -1
	s_cbranch_scc0 .LBB0_876
	s_mov_b32 s10, m0
	s_mov_b32 m0, s67
	s_nop 0
	global_load_lds_dwordx4 v169, s[8:9]
	s_mov_b32 m0, s10
	s_add_i32 s50, s67, 0x800
	s_mov_b32 s10, m0
	s_mov_b32 m0, s68
	s_nop 0
	global_load_lds_dwordx4 v170, s[8:9]
	s_mov_b32 m0, s10
	s_add_i32 s51, s67, 0xc00
	s_mov_b32 s10, m0
	s_mov_b32 m0, s50
	s_nop 0
	global_load_lds_dwordx4 v174, s[8:9]
	s_mov_b32 m0, s10
	s_add_i32 s69, s67, 0x1000
	s_mov_b32 s10, m0
	s_mov_b32 m0, s51
	s_nop 0
	global_load_lds_dwordx4 v175, s[8:9]
	s_mov_b32 m0, s10
	s_add_i32 s70, s67, 0x1400
	s_mov_b32 s10, m0
	s_mov_b32 m0, s69
	s_nop 0
	global_load_lds_dwordx4 v176, s[8:9]
	s_mov_b32 m0, s10
	v_mov_b32_e32 v26, 0
	s_mov_b32 s10, m0
	s_mov_b32 m0, s70
	s_nop 0
	global_load_lds_dwordx4 v177, s[8:9]
	s_mov_b32 m0, s10
	ds_read_b128 v[228:231], v248 offset:8192
	ds_read_b128 v[232:235], v248 offset:9216
	ds_read_b128 v[236:239], v248 offset:10240
	ds_read_b128 v[240:243], v248 offset:11264
	ds_read_b128 v[60:63], v248 offset:12288
	ds_read_b128 v[64:67], v248 offset:13312
	ds_read_b128 v[68:71], v248 offset:14336
	ds_read_b128 v[72:75], v248 offset:15360
	s_waitcnt lgkmcnt(0)
	s_waitcnt vmcnt(10)
	v_mov_b32_e32 v106, v60
	v_mov_b32_e32 v107, v61
	v_mov_b32_e32 v108, v62
	v_mov_b32_e32 v109, v63
	v_mov_b32_e32 v102, v64
	v_mov_b32_e32 v103, v65
	v_mov_b32_e32 v104, v66
	v_mov_b32_e32 v105, v67
	v_mov_b32_e32 v110, v68
	v_mov_b32_e32 v111, v69
	v_mov_b32_e32 v112, v70
	v_mov_b32_e32 v113, v71
	v_mov_b32_e32 v98, v72
	v_mov_b32_e32 v99, v73
	v_mov_b32_e32 v100, v74
	v_mov_b32_e32 v101, v75
	v_xor_b32_e32 v139, 64, v172
	v_cvt_pk_bf16_f32 v2, v228, v229
	v_cvt_pk_bf16_f32 v3, v230, v231
	v_lshlrev_b32_e32 v4, 5, v134
	v_add_u32_e32 v135, v173, v4
	v_xor_b32_e32 v5, 32, v4
	ds_write_b64 v135, v[2:3]
	v_cvt_pk_bf16_f32 v2, v232, v233
	v_cvt_pk_bf16_f32 v3, v234, v235
	v_add_u32_e32 v136, v173, v5
	v_xor_b32_e32 v5, 64, v4
	ds_write_b64 v136, v[2:3] offset:256
	v_cvt_pk_bf16_f32 v2, v236, v237
	v_cvt_pk_bf16_f32 v3, v238, v239
	v_add_u32_e32 v137, v173, v5
	v_xor_b32_e32 v4, 0x60, v4
	ds_write_b64 v137, v[2:3] offset:512
	v_cvt_pk_bf16_f32 v2, v240, v241
	v_cvt_pk_bf16_f32 v3, v242, v243
	v_add_u32_e32 v138, v173, v4
	ds_write_b64 v138, v[2:3] offset:768
	global_load_dwordx4 v[122:125], v168, s[36:37]
	global_load_dwordx4 v[118:121], v168, s[36:37] offset:2048
	global_load_dwordx4 v[126:129], v168, s[38:39]
	global_load_dwordx4 v[114:117], v168, s[38:39] offset:2048
	s_waitcnt lgkmcnt(0)
	s_barrier
	v_add_u32_e32 v2, 0x2000, v172
	s_add_i32 s71, s67, 0x2000
	v_xor_b32_e32 v140, 64, v2
	v_xor_b32_e32 v141, 32, v171
	v_xor_b32_e32 v142, 64, v171
	v_xor_b32_e32 v143, 0x60, v171
	v_xor_b32_e32 v144, 0x80, v171
	v_xor_b32_e32 v145, 0xa0, v171
	v_xor_b32_e32 v146, 0xc0, v171
	s_add_i32 s72, s67, 0x2400
	v_xor_b32_e32 v147, 0xe0, v171
	s_add_i32 s73, s67, 0x2800
	s_add_i32 s74, s67, 0x2c00
	s_add_i32 s75, s67, 0x3000
	s_add_i32 s76, s67, 0x3400
	s_mov_b32 s48, 0
	s_mov_b64 s[14:15], 0
	v_mov_b32_e32 v27, v26
	v_mov_b32_e32 v28, v26
	v_mov_b32_e32 v29, v26
	v_mov_b32_e32 v2, v26
	v_mov_b32_e32 v3, v26
	v_mov_b32_e32 v4, v26
	v_mov_b32_e32 v5, v26
	v_mov_b32_e32 v10, v26
	v_mov_b32_e32 v11, v26
	v_mov_b32_e32 v12, v26
	v_mov_b32_e32 v13, v26
	v_mov_b32_e32 v50, v26
	v_mov_b32_e32 v51, v26
	v_mov_b32_e32 v52, v26
	v_mov_b32_e32 v53, v26
	v_mov_b32_e32 v14, v26
	v_mov_b32_e32 v15, v26
	v_mov_b32_e32 v16, v26
	v_mov_b32_e32 v17, v26
	v_mov_b32_e32 v30, v26
	v_mov_b32_e32 v31, v26
	v_mov_b32_e32 v32, v26
	v_mov_b32_e32 v33, v26
	v_mov_b32_e32 v66, v26
	v_mov_b32_e32 v67, v26
	v_mov_b32_e32 v68, v26
	v_mov_b32_e32 v69, v26
	v_mov_b32_e32 v34, v26
	v_mov_b32_e32 v35, v26
	v_mov_b32_e32 v36, v26
	v_mov_b32_e32 v37, v26
	v_mov_b32_e32 v62, v26
	v_mov_b32_e32 v63, v26
	v_mov_b32_e32 v64, v26
	v_mov_b32_e32 v65, v26
	v_mov_b32_e32 v82, v26
	v_mov_b32_e32 v83, v26
	v_mov_b32_e32 v84, v26
	v_mov_b32_e32 v85, v26
	v_mov_b32_e32 v54, v26
	v_mov_b32_e32 v55, v26
	v_mov_b32_e32 v56, v26
	v_mov_b32_e32 v57, v26
	v_mov_b32_e32 v86, v26
	v_mov_b32_e32 v87, v26
	v_mov_b32_e32 v88, v26
	v_mov_b32_e32 v89, v26
	v_mov_b32_e32 v22, v26
	v_mov_b32_e32 v23, v26
	v_mov_b32_e32 v24, v26
	v_mov_b32_e32 v25, v26
	v_mov_b32_e32 v6, v26
	v_mov_b32_e32 v7, v26
	v_mov_b32_e32 v8, v26
	v_mov_b32_e32 v9, v26
	v_mov_b32_e32 v42, v26
	v_mov_b32_e32 v43, v26
	v_mov_b32_e32 v44, v26
	v_mov_b32_e32 v45, v26
	v_mov_b32_e32 v38, v26
	v_mov_b32_e32 v39, v26
	v_mov_b32_e32 v40, v26
	v_mov_b32_e32 v41, v26
	v_mov_b32_e32 v18, v26
	v_mov_b32_e32 v19, v26
	v_mov_b32_e32 v20, v26
	v_mov_b32_e32 v21, v26
	v_mov_b32_e32 v70, v26
	v_mov_b32_e32 v71, v26
	v_mov_b32_e32 v72, v26
	v_mov_b32_e32 v73, v26
	v_mov_b32_e32 v58, v26
	v_mov_b32_e32 v59, v26
	v_mov_b32_e32 v60, v26
	v_mov_b32_e32 v61, v26
	v_mov_b32_e32 v46, v26
	v_mov_b32_e32 v47, v26
	v_mov_b32_e32 v48, v26
	v_mov_b32_e32 v49, v26
	v_mov_b32_e32 v90, v26
	v_mov_b32_e32 v91, v26
	v_mov_b32_e32 v92, v26
	v_mov_b32_e32 v93, v26
	v_mov_b32_e32 v78, v26
	v_mov_b32_e32 v79, v26
	v_mov_b32_e32 v80, v26
	v_mov_b32_e32 v81, v26
	v_mov_b32_e32 v74, v26
	v_mov_b32_e32 v75, v26
	v_mov_b32_e32 v76, v26
	v_mov_b32_e32 v77, v26
	v_mov_b32_e32 v94, v26
	v_mov_b32_e32 v95, v26
	v_mov_b32_e32 v96, v26
	v_mov_b32_e32 v97, v26

.LBB0_877:
	s_mov_b32 s10, m0
	s_mov_b32 m0, s67
	s_nop 0
	global_load_lds_dwordx4 v169, s[8:9]
	s_mov_b32 m0, s10
	s_add_i32 s69, s67, 0x800
	s_mov_b32 s10, m0
	s_mov_b32 m0, s68
	s_nop 0
	global_load_lds_dwordx4 v170, s[8:9]
	s_mov_b32 m0, s10
	s_add_i32 s70, s67, 0xc00
	s_mov_b32 s10, m0
	s_mov_b32 m0, s69
	s_nop 0
	global_load_lds_dwordx4 v174, s[8:9]
	s_mov_b32 m0, s10
	v_xor_b32_e32 v102, 64, v172
	s_mov_b32 s10, m0
	s_mov_b32 m0, s70
	s_nop 0
	global_load_lds_dwordx4 v175, s[8:9]
	s_mov_b32 m0, s10
	ds_read_b128 v[228:231], v248 offset:8192
	ds_read_b128 v[232:235], v248 offset:9216
	ds_read_b128 v[236:239], v248 offset:10240
	ds_read_b128 v[240:243], v248 offset:11264
	ds_read_b128 v[60:63], v248 offset:12288
	ds_read_b128 v[64:67], v248 offset:13312
	ds_read_b128 v[68:71], v248 offset:14336
	ds_read_b128 v[72:75], v248 offset:15360
	s_waitcnt lgkmcnt(0)
	s_waitcnt vmcnt(8)
	v_mov_b32_e32 v38, v60
	v_mov_b32_e32 v39, v61
	v_mov_b32_e32 v40, v62
	v_mov_b32_e32 v41, v63
	v_mov_b32_e32 v26, v64
	v_mov_b32_e32 v27, v65
	v_mov_b32_e32 v28, v66
	v_mov_b32_e32 v29, v67
	v_mov_b32_e32 v50, v68
	v_mov_b32_e32 v51, v69
	v_mov_b32_e32 v52, v70
	v_mov_b32_e32 v53, v71
	v_mov_b32_e32 v22, v72
	v_mov_b32_e32 v23, v73
	v_mov_b32_e32 v24, v74
	v_mov_b32_e32 v25, v75
	s_add_i32 s71, s67, 0x2000
	v_cvt_pk_bf16_f32 v2, v228, v229
	v_cvt_pk_bf16_f32 v3, v230, v231
	v_lshlrev_b32_e32 v4, 5, v134
	v_add_u32_e32 v98, v173, v4
	v_xor_b32_e32 v5, 32, v4
	ds_write_b64 v98, v[2:3]
	v_cvt_pk_bf16_f32 v2, v232, v233
	v_cvt_pk_bf16_f32 v3, v234, v235
	v_add_u32_e32 v99, v173, v5
	v_xor_b32_e32 v5, 64, v4
	ds_write_b64 v99, v[2:3] offset:256
	v_cvt_pk_bf16_f32 v2, v236, v237
	v_cvt_pk_bf16_f32 v3, v238, v239
	v_add_u32_e32 v100, v173, v5
	v_xor_b32_e32 v4, 0x60, v4
	ds_write_b64 v100, v[2:3] offset:512
	v_cvt_pk_bf16_f32 v2, v240, v241
	v_cvt_pk_bf16_f32 v3, v242, v243
	v_add_u32_e32 v101, v173, v4
	ds_write_b64 v101, v[2:3] offset:768
	global_load_dwordx4 v[78:81], v168, s[36:37]
	global_load_dwordx4 v[66:69], v168, s[36:37] offset:2048
	global_load_dwordx4 v[82:85], v168, s[38:39]
	global_load_dwordx4 v[58:61], v168, s[38:39] offset:2048
	s_waitcnt lgkmcnt(0)
	s_barrier
	v_add_u32_e32 v2, 0x2000, v172
	v_xor_b32_e32 v103, 64, v2
	v_mov_b32_e32 v2, 0
	v_xor_b32_e32 v104, 32, v171
	v_xor_b32_e32 v105, 64, v171
	v_xor_b32_e32 v106, 0x60, v171
	v_xor_b32_e32 v107, 0x80, v171
	v_xor_b32_e32 v108, 0xa0, v171
	v_xor_b32_e32 v109, 0xc0, v171
	s_add_i32 s72, s67, 0x2400
	v_xor_b32_e32 v110, 0xe0, v171
	s_add_i32 s73, s67, 0x2800
	s_add_i32 s74, s67, 0x2c00
	s_mov_b32 s50, 0
	s_mov_b64 s[46:47], 0
	v_mov_b32_e32 v3, v2
	v_mov_b32_e32 v4, v2
	v_mov_b32_e32 v5, v2
	v_mov_b32_e32 v10, v2
	v_mov_b32_e32 v11, v2
	v_mov_b32_e32 v12, v2
	v_mov_b32_e32 v13, v2
	v_mov_b32_e32 v14, v2
	v_mov_b32_e32 v15, v2
	v_mov_b32_e32 v16, v2
	v_mov_b32_e32 v17, v2
	v_mov_b32_e32 v30, v2
	v_mov_b32_e32 v31, v2
	v_mov_b32_e32 v32, v2
	v_mov_b32_e32 v33, v2
	v_mov_b32_e32 v34, v2
	v_mov_b32_e32 v35, v2
	v_mov_b32_e32 v36, v2
	v_mov_b32_e32 v37, v2
	v_mov_b32_e32 v62, v2
	v_mov_b32_e32 v63, v2
	v_mov_b32_e32 v64, v2
	v_mov_b32_e32 v65, v2
	v_mov_b32_e32 v54, v2
	v_mov_b32_e32 v55, v2
	v_mov_b32_e32 v56, v2
	v_mov_b32_e32 v57, v2
	v_mov_b32_e32 v86, v2
	v_mov_b32_e32 v87, v2
	v_mov_b32_e32 v88, v2
	v_mov_b32_e32 v89, v2
	v_mov_b32_e32 v6, v2
	v_mov_b32_e32 v7, v2
	v_mov_b32_e32 v8, v2
	v_mov_b32_e32 v9, v2
	v_mov_b32_e32 v42, v2
	v_mov_b32_e32 v43, v2
	v_mov_b32_e32 v44, v2
	v_mov_b32_e32 v45, v2
	v_mov_b32_e32 v18, v2
	v_mov_b32_e32 v19, v2
	v_mov_b32_e32 v20, v2
	v_mov_b32_e32 v21, v2
	v_mov_b32_e32 v70, v2
	v_mov_b32_e32 v71, v2
	v_mov_b32_e32 v72, v2
	v_mov_b32_e32 v73, v2
	v_mov_b32_e32 v46, v2
	v_mov_b32_e32 v47, v2
	v_mov_b32_e32 v48, v2
	v_mov_b32_e32 v49, v2
	v_mov_b32_e32 v90, v2
	v_mov_b32_e32 v91, v2
	v_mov_b32_e32 v92, v2
	v_mov_b32_e32 v93, v2
	v_mov_b32_e32 v74, v2
	v_mov_b32_e32 v75, v2
	v_mov_b32_e32 v76, v2
	v_mov_b32_e32 v77, v2
	v_mov_b32_e32 v94, v2
	v_mov_b32_e32 v95, v2
	v_mov_b32_e32 v96, v2
	v_mov_b32_e32 v97, v2

.LBB0_883:
	v_mov_b32_e32 v125, 0
	v_lshlrev_b32_e32 v98, 5, v134
	v_add_u32_e32 v99, 0x2000, v172
	s_andn2_b64 vcc, exec, s[14:15]
	v_xor_b32_e32 v178, 64, v172
	v_xor_b32_e32 v179, 32, v171
	v_xor_b32_e32 v180, 64, v171
	v_xor_b32_e32 v181, 0x60, v171
	v_xor_b32_e32 v182, 0x80, v171
	v_xor_b32_e32 v183, 0xa0, v171
	v_xor_b32_e32 v184, 0xc0, v171
	v_xor_b32_e32 v185, 0xe0, v171
	v_add_u32_e32 v186, v173, v98
	v_xor_b32_e32 v190, 32, v98
	v_xor_b32_e32 v189, 64, v98
	v_xor_b32_e32 v188, 0x60, v98
	v_xor_b32_e32 v187, 64, v99
	v_mov_b32_e32 v124, v125
	v_mov_b32_e32 v123, v125
	v_mov_b32_e32 v122, v125
	v_mov_b32_e32 v117, v125
	v_mov_b32_e32 v116, v125
	v_mov_b32_e32 v115, v125
	v_mov_b32_e32 v114, v125
	v_mov_b32_e32 v109, v125
	v_mov_b32_e32 v108, v125
	v_mov_b32_e32 v107, v125
	v_mov_b32_e32 v106, v125
	v_mov_b32_e32 v105, v125
	v_mov_b32_e32 v104, v125
	v_mov_b32_e32 v103, v125
	v_mov_b32_e32 v102, v125
	v_mov_b32_e32 v129, v125
	v_mov_b32_e32 v128, v125
	v_mov_b32_e32 v127, v125
	v_mov_b32_e32 v126, v125
	v_mov_b32_e32 v121, v125
	v_mov_b32_e32 v120, v125
	v_mov_b32_e32 v119, v125
	v_mov_b32_e32 v118, v125
	v_mov_b32_e32 v113, v125
	v_mov_b32_e32 v112, v125
	v_mov_b32_e32 v111, v125
	v_mov_b32_e32 v110, v125
	v_mov_b32_e32 v101, v125
	v_mov_b32_e32 v100, v125
	v_mov_b32_e32 v99, v125
	v_mov_b32_e32 v98, v125
	s_cbranch_vccnz .LBB0_887
	s_waitcnt vmcnt(13)
	v_lshlrev_b32_e32 v2, 8, v131
	v_and_or_b32 v191, v2, s60, v133
	s_waitcnt vmcnt(12)
	v_lshlrev_b32_e32 v2, 8, v130
	v_and_or_b32 v192, v2, s60, v132
	s_mov_b32 s10, m0
	s_mov_b32 m0, s67
	s_nop 0
	global_load_lds_dwordx4 v169, s[8:9]
	s_mov_b32 m0, s10
	s_add_i32 s48, s67, 0x800
	s_mov_b32 s10, m0
	s_mov_b32 m0, s68
	s_nop 0
	global_load_lds_dwordx4 v170, s[8:9]
	s_mov_b32 m0, s10
	s_add_i32 s49, s67, 0xc00
	s_mov_b32 s10, m0
	s_mov_b32 m0, s48
	s_nop 0
	global_load_lds_dwordx4 v174, s[8:9]
	s_mov_b32 m0, s10
	s_add_i32 s50, s67, 0x1000
	s_mov_b32 s10, m0
	s_mov_b32 m0, s49
	s_nop 0
	global_load_lds_dwordx4 v175, s[8:9]
	s_mov_b32 m0, s10
	s_add_i32 s51, s67, 0x1400
	s_mov_b32 s10, m0
	s_mov_b32 m0, s50
	s_nop 0
	global_load_lds_dwordx4 v176, s[8:9]
	s_mov_b32 m0, s10
	s_add_i32 s69, s67, 0x1800
	s_mov_b32 s10, m0
	s_mov_b32 m0, s51
	s_nop 0
	global_load_lds_dwordx4 v177, s[8:9]
	s_mov_b32 m0, s10
	s_add_i32 s70, s67, 0x1c00
	s_mov_b32 s10, m0
	s_mov_b32 m0, s69
	s_nop 0
	global_load_lds_dwordx4 v191, s[8:9]
	s_mov_b32 m0, s10
	v_add_u32_e32 v193, v173, v190
	s_mov_b32 s10, m0
	s_mov_b32 m0, s70
	s_nop 0
	global_load_lds_dwordx4 v192, s[8:9]
	s_mov_b32 m0, s10
	ds_read_b128 v[228:231], v248 offset:8192
	ds_read_b128 v[232:235], v248 offset:9216
	ds_read_b128 v[236:239], v248 offset:10240
	ds_read_b128 v[240:243], v248 offset:11264
	ds_read_b128 v[60:63], v248 offset:12288
	ds_read_b128 v[64:67], v248 offset:13312
	ds_read_b128 v[68:71], v248 offset:14336
	ds_read_b128 v[72:75], v248 offset:15360
	s_waitcnt lgkmcnt(0)
	s_waitcnt vmcnt(12)
	v_mov_b32_e32 v138, v60
	v_mov_b32_e32 v139, v61
	v_mov_b32_e32 v140, v62
	v_mov_b32_e32 v141, v63
	v_mov_b32_e32 v134, v64
	v_mov_b32_e32 v135, v65
	v_mov_b32_e32 v136, v66
	v_mov_b32_e32 v137, v67
	v_mov_b32_e32 v142, v68
	v_mov_b32_e32 v143, v69
	v_mov_b32_e32 v144, v70
	v_mov_b32_e32 v145, v71
	v_mov_b32_e32 v130, v72
	v_mov_b32_e32 v131, v73
	v_mov_b32_e32 v132, v74
	v_mov_b32_e32 v133, v75
	v_add_u32_e32 v194, v173, v189
	v_cvt_pk_bf16_f32 v2, v228, v229
	v_cvt_pk_bf16_f32 v3, v230, v231
	ds_write_b64 v186, v[2:3]
	v_cvt_pk_bf16_f32 v2, v232, v233
	v_cvt_pk_bf16_f32 v3, v234, v235
	ds_write_b64 v193, v[2:3] offset:256
	v_cvt_pk_bf16_f32 v2, v236, v237
	v_cvt_pk_bf16_f32 v3, v238, v239
	ds_write_b64 v194, v[2:3] offset:512
	v_cvt_pk_bf16_f32 v2, v240, v241
	v_cvt_pk_bf16_f32 v3, v242, v243
	v_add_u32_e32 v195, v173, v188
	ds_write_b64 v195, v[2:3] offset:768
	global_load_dwordx4 v[154:157], v168, s[36:37]
	global_load_dwordx4 v[150:153], v168, s[36:37] offset:2048
	global_load_dwordx4 v[158:161], v168, s[38:39]
	global_load_dwordx4 v[146:149], v168, s[38:39] offset:2048
	s_waitcnt lgkmcnt(0)
	s_barrier
	v_mov_b32_e32 v98, 0
	s_add_i32 s71, s67, 0x2000
	s_add_i32 s72, s67, 0x2400
	s_add_i32 s73, s67, 0x2800
	s_add_i32 s74, s67, 0x2c00
	s_add_i32 s75, s67, 0x3000
	s_add_i32 s76, s67, 0x3400
	s_add_i32 s77, s67, 0x3800
	s_add_i32 s78, s67, 0x3c00
	s_mov_b32 s46, 0
	s_mov_b64 s[12:13], 0
	v_mov_b32_e32 v99, v98
	v_mov_b32_e32 v100, v98
	v_mov_b32_e32 v101, v98
	v_mov_b32_e32 v26, v98
	v_mov_b32_e32 v27, v98
	v_mov_b32_e32 v28, v98
	v_mov_b32_e32 v29, v98
	v_mov_b32_e32 v2, v98
	v_mov_b32_e32 v3, v98
	v_mov_b32_e32 v4, v98
	v_mov_b32_e32 v5, v98
	v_mov_b32_e32 v10, v98
	v_mov_b32_e32 v11, v98
	v_mov_b32_e32 v12, v98
	v_mov_b32_e32 v13, v98
	v_mov_b32_e32 v110, v98
	v_mov_b32_e32 v111, v98
	v_mov_b32_e32 v112, v98
	v_mov_b32_e32 v113, v98
	v_mov_b32_e32 v50, v98
	v_mov_b32_e32 v51, v98
	v_mov_b32_e32 v52, v98
	v_mov_b32_e32 v53, v98
	v_mov_b32_e32 v14, v98
	v_mov_b32_e32 v15, v98
	v_mov_b32_e32 v16, v98
	v_mov_b32_e32 v17, v98
	v_mov_b32_e32 v30, v98
	v_mov_b32_e32 v31, v98
	v_mov_b32_e32 v32, v98
	v_mov_b32_e32 v33, v98
	v_mov_b32_e32 v118, v98
	v_mov_b32_e32 v119, v98
	v_mov_b32_e32 v120, v98
	v_mov_b32_e32 v121, v98
	v_mov_b32_e32 v66, v98
	v_mov_b32_e32 v67, v98
	v_mov_b32_e32 v68, v98
	v_mov_b32_e32 v69, v98
	v_mov_b32_e32 v34, v98
	v_mov_b32_e32 v35, v98
	v_mov_b32_e32 v36, v98
	v_mov_b32_e32 v37, v98
	v_mov_b32_e32 v62, v98
	v_mov_b32_e32 v63, v98
	v_mov_b32_e32 v64, v98
	v_mov_b32_e32 v65, v98
	v_mov_b32_e32 v126, v98
	v_mov_b32_e32 v127, v98
	v_mov_b32_e32 v128, v98
	v_mov_b32_e32 v129, v98
	v_mov_b32_e32 v82, v98
	v_mov_b32_e32 v83, v98
	v_mov_b32_e32 v84, v98
	v_mov_b32_e32 v85, v98
	v_mov_b32_e32 v54, v98
	v_mov_b32_e32 v55, v98
	v_mov_b32_e32 v56, v98
	v_mov_b32_e32 v57, v98
	v_mov_b32_e32 v86, v98
	v_mov_b32_e32 v87, v98
	v_mov_b32_e32 v88, v98
	v_mov_b32_e32 v89, v98
	v_mov_b32_e32 v102, v98
	v_mov_b32_e32 v103, v98
	v_mov_b32_e32 v104, v98
	v_mov_b32_e32 v105, v98
	v_mov_b32_e32 v22, v98
	v_mov_b32_e32 v23, v98
	v_mov_b32_e32 v24, v98
	v_mov_b32_e32 v25, v98
	v_mov_b32_e32 v6, v98
	v_mov_b32_e32 v7, v98
	v_mov_b32_e32 v8, v98
	v_mov_b32_e32 v9, v98
	v_mov_b32_e32 v42, v98
	v_mov_b32_e32 v43, v98
	v_mov_b32_e32 v44, v98
	v_mov_b32_e32 v45, v98
	v_mov_b32_e32 v106, v98
	v_mov_b32_e32 v107, v98
	v_mov_b32_e32 v108, v98
	v_mov_b32_e32 v109, v98
	v_mov_b32_e32 v38, v98
	v_mov_b32_e32 v39, v98
	v_mov_b32_e32 v40, v98
	v_mov_b32_e32 v41, v98
	v_mov_b32_e32 v18, v98
	v_mov_b32_e32 v19, v98
	v_mov_b32_e32 v20, v98
	v_mov_b32_e32 v21, v98
	v_mov_b32_e32 v70, v98
	v_mov_b32_e32 v71, v98
	v_mov_b32_e32 v72, v98
	v_mov_b32_e32 v73, v98
	v_mov_b32_e32 v114, v98
	v_mov_b32_e32 v115, v98
	v_mov_b32_e32 v116, v98
	v_mov_b32_e32 v117, v98
	v_mov_b32_e32 v58, v98
	v_mov_b32_e32 v59, v98
	v_mov_b32_e32 v60, v98
	v_mov_b32_e32 v61, v98
	v_mov_b32_e32 v46, v98
	v_mov_b32_e32 v47, v98
	v_mov_b32_e32 v48, v98
	v_mov_b32_e32 v49, v98
	v_mov_b32_e32 v90, v98
	v_mov_b32_e32 v91, v98
	v_mov_b32_e32 v92, v98
	v_mov_b32_e32 v93, v98
	v_mov_b32_e32 v122, v98
	v_mov_b32_e32 v123, v98
	v_mov_b32_e32 v124, v98
	v_mov_b32_e32 v125, v98
	v_mov_b32_e32 v78, v98
	v_mov_b32_e32 v79, v98
	v_mov_b32_e32 v80, v98
	v_mov_b32_e32 v81, v98
	v_mov_b32_e32 v74, v98
	v_mov_b32_e32 v75, v98
	v_mov_b32_e32 v76, v98
	v_mov_b32_e32 v77, v98
	v_mov_b32_e32 v94, v98
	v_mov_b32_e32 v95, v98
	v_mov_b32_e32 v96, v98
	v_mov_b32_e32 v97, v98

.LBB0_887:
	s_and_b64 vcc, exec, s[12:13]
	s_cbranch_vccz .LBB0_891
	s_mov_b32 s10, m0
	s_mov_b32 m0, s67
	s_nop 0
	global_load_lds_dwordx4 v169, s[8:9]
	s_mov_b32 m0, s10
	v_add_u32_e32 v47, v173, v189
	s_mov_b32 s10, m0
	s_mov_b32 m0, s68
	s_nop 0
	global_load_lds_dwordx4 v170, s[8:9]
	s_mov_b32 m0, s10
	ds_read_b128 v[228:231], v248 offset:8192
	ds_read_b128 v[232:235], v248 offset:9216
	ds_read_b128 v[236:239], v248 offset:10240
	ds_read_b128 v[240:243], v248 offset:11264
	ds_read_b128 v[60:63], v248 offset:12288
	ds_read_b128 v[64:67], v248 offset:13312
	ds_read_b128 v[68:71], v248 offset:14336
	ds_read_b128 v[72:75], v248 offset:15360
	s_waitcnt lgkmcnt(0)
	s_waitcnt vmcnt(6)
	v_mov_b32_e32 v18, v60
	v_mov_b32_e32 v19, v61
	v_mov_b32_e32 v20, v62
	v_mov_b32_e32 v21, v63
	v_mov_b32_e32 v6, v64
	v_mov_b32_e32 v7, v65
	v_mov_b32_e32 v8, v66
	v_mov_b32_e32 v9, v67
	v_mov_b32_e32 v14, v68
	v_mov_b32_e32 v15, v69
	v_mov_b32_e32 v16, v70
	v_mov_b32_e32 v17, v71
	v_mov_b32_e32 v2, v72
	v_mov_b32_e32 v3, v73
	v_mov_b32_e32 v4, v74
	v_mov_b32_e32 v5, v75
	v_add_u32_e32 v46, v173, v190
	v_cvt_pk_bf16_f32 v10, v228, v229
	v_cvt_pk_bf16_f32 v11, v230, v231
	ds_write_b64 v186, v[10:11]
	v_cvt_pk_bf16_f32 v10, v236, v237
	v_cvt_pk_bf16_f32 v11, v238, v239
	v_cvt_pk_bf16_f32 v12, v232, v233
	v_cvt_pk_bf16_f32 v13, v234, v235
	ds_write_b64 v47, v[10:11] offset:512
	v_cvt_pk_bf16_f32 v10, v240, v241
	v_cvt_pk_bf16_f32 v11, v242, v243
	v_add_u32_e32 v48, v173, v188
	ds_write_b64 v46, v[12:13] offset:256
	ds_write_b64 v48, v[10:11] offset:768
	global_load_dwordx4 v[38:41], v168, s[36:37]
	global_load_dwordx4 v[26:29], v168, s[36:37] offset:2048
	global_load_dwordx4 v[34:37], v168, s[38:39]
	global_load_dwordx4 v[22:25], v168, s[38:39] offset:2048
	s_waitcnt lgkmcnt(0)
	s_barrier
	v_mov_b32_e32 v10, 0
	s_add_i32 s46, s67, 0x2000
	s_add_i32 s47, s67, 0x2400
	s_mov_b32 s48, 0
	s_mov_b64 s[12:13], 0
	v_mov_b32_e32 v11, v10
	v_mov_b32_e32 v12, v10
	v_mov_b32_e32 v13, v10
	v_mov_b32_e32 v30, v10
	v_mov_b32_e32 v31, v10
	v_mov_b32_e32 v32, v10
	v_mov_b32_e32 v33, v10
	v_mov_b32_e32 v62, v10
	v_mov_b32_e32 v63, v10
	v_mov_b32_e32 v64, v10
	v_mov_b32_e32 v65, v10
	v_mov_b32_e32 v86, v10
	v_mov_b32_e32 v87, v10
	v_mov_b32_e32 v88, v10
	v_mov_b32_e32 v89, v10
	v_mov_b32_e32 v42, v10
	v_mov_b32_e32 v43, v10
	v_mov_b32_e32 v44, v10
	v_mov_b32_e32 v45, v10
	v_mov_b32_e32 v70, v10
	v_mov_b32_e32 v71, v10
	v_mov_b32_e32 v72, v10
	v_mov_b32_e32 v73, v10
	v_mov_b32_e32 v90, v10
	v_mov_b32_e32 v91, v10
	v_mov_b32_e32 v92, v10
	v_mov_b32_e32 v93, v10
	v_mov_b32_e32 v94, v10
	v_mov_b32_e32 v95, v10
	v_mov_b32_e32 v96, v10
	v_mov_b32_e32 v97, v10

.Lmy_none_be:
	s_mov_b32 s99, 0
	s_nop 0
	v_readfirstlane_b32 s10, v162
	s_ashr_i32 s10, s10, 6
	s_mul_i32 s66, s66, s10
	v_and_or_b32 v131, v162, 15, s64
	v_lshrrev_b32_e32 v130, 2, v162
	s_lshl_b32 s48, s66, 4
	v_and_b32_e32 v130, 12, v130
	v_add_u32_e32 v132, s48, v131
	v_cmp_gt_i32_e32 vcc, s65, v132
	v_lshlrev_b32_e32 v162, 1, v130
	s_and_saveexec_b64 s[46:47], vcc
	s_cbranch_execz .LBB0_893
	s_add_i32 s99, s99, 4
	v_ashrrev_i32_e32 v133, 31, v132
	v_lshl_add_u64 v[134:135], v[132:133], 2, s[26:27]
	v_mul_f32_e32 v134, 0xbfb8aa3b, v94
	v_mul_f32_e32 v135, 0xbfb8aa3b, v95
	v_exp_f32_e32 v134, v134
	v_exp_f32_e32 v135, v135
	v_mul_f32_e32 v136, 0xbfb8aa3b, v96
	v_mul_f32_e32 v137, 0xbfb8aa3b, v97
	v_exp_f32_e32 v136, v136
	v_exp_f32_e32 v137, v137
	v_pk_add_f32 v[134:135], v[134:135], 1.0 op_sel_hi:[1,0]
	v_mul_f32_e32 v138, 0xbfb8aa3b, v90
	v_pk_add_f32 v[136:137], v[136:137], 1.0 op_sel_hi:[1,0]
	v_mul_f32_e32 v139, 0xbfb8aa3b, v91
	v_exp_f32_e32 v138, v138
	v_exp_f32_e32 v139, v139
	v_rcp_f32_e32 v140, v135
	s_nop 0
	v_mul_f32_e32 v95, v95, v140
	v_rcp_f32_e32 v135, v134
	s_nop 0
	v_mul_f32_e32 v94, v94, v135
	v_pk_mul_f32 v[86:87], v[86:87], v[94:95]
	v_pk_add_f32 v[138:139], v[138:139], 1.0 op_sel_hi:[1,0]
	v_rcp_f32_e32 v134, v137
	s_nop 0
	v_mul_f32_e32 v95, v97, v134
	v_rcp_f32_e32 v94, v136
	s_nop 0
	v_mul_f32_e32 v94, v96, v94
	v_add_u32_e32 v132, s63, v132
	v_pk_mul_f32 v[88:89], v[88:89], v[94:95]
	v_ashrrev_i32_e32 v133, 31, v132
	v_lshlrev_b64 v[132:133], 9, v[132:133]
	v_lshl_add_u64 v[132:133], s[20:21], 0, v[132:133]
	v_mov_b32_e32 v130, v244
	v_pk_mul_f32 v[86:87], v[86:87], v[130:131] op_sel_hi:[1,0]
	v_pk_mul_f32 v[88:89], v[88:89], v[130:131] op_sel_hi:[1,0]
	v_lshl_add_u64 v[132:133], v[132:133], 0, v[162:163]
	v_cvt_pk_bf16_f32 v86, v86, v87
	v_cvt_pk_bf16_f32 v87, v88, v89
	global_store_dwordx2 v[132:133], v[86:87], off
	v_rcp_f32_e32 v86, v139
	s_nop 0
	v_mul_f32_e32 v87, v91, v86
	v_mul_f32_e32 v88, 0xbfb8aa3b, v92
	v_mul_f32_e32 v89, 0xbfb8aa3b, v93
	v_exp_f32_e32 v88, v88
	v_exp_f32_e32 v89, v89
	v_rcp_f32_e32 v86, v138
	s_nop 0
	v_mul_f32_e32 v86, v90, v86
	v_pk_mul_f32 v[62:63], v[62:63], v[86:87]
	v_pk_add_f32 v[88:89], v[88:89], 1.0 op_sel_hi:[1,0]
	v_pk_mul_f32 v[62:63], v[62:63], v[130:131] op_sel_hi:[1,0]
	v_cvt_pk_bf16_f32 v62, v62, v63
	v_rcp_f32_e32 v63, v89
	s_nop 0
	v_mul_f32_e32 v87, v93, v63
	v_mul_f32_e32 v89, 0xbfb8aa3b, v70
	v_exp_f32_e32 v90, v89
	v_mul_f32_e32 v89, 0xbfb8aa3b, v71
	v_exp_f32_e32 v91, v89
	v_rcp_f32_e32 v63, v88
	s_nop 0
	v_mul_f32_e32 v86, v92, v63
	v_pk_mul_f32 v[64:65], v[64:65], v[86:87]
	v_pk_add_f32 v[86:87], v[90:91], 1.0 op_sel_hi:[1,0]
	v_pk_mul_f32 v[64:65], v[64:65], v[130:131] op_sel_hi:[1,0]
	v_cvt_pk_bf16_f32 v63, v64, v65
	global_store_dwordx2 v[132:133], v[62:63], off offset:32
	v_rcp_f32_e32 v62, v87
	s_nop 0
	v_mul_f32_e32 v63, v71, v62
	v_mul_f32_e32 v64, 0xbfb8aa3b, v72
	v_mul_f32_e32 v65, 0xbfb8aa3b, v73
	v_exp_f32_e32 v64, v64
	v_exp_f32_e32 v65, v65
	v_rcp_f32_e32 v62, v86
	s_nop 0
	v_mul_f32_e32 v62, v70, v62
	v_pk_mul_f32 v[30:31], v[30:31], v[62:63]
	v_pk_add_f32 v[64:65], v[64:65], 1.0 op_sel_hi:[1,0]
	v_pk_mul_f32 v[30:31], v[30:31], v[130:131] op_sel_hi:[1,0]
	v_cvt_pk_bf16_f32 v30, v30, v31
	v_rcp_f32_e32 v31, v65
	s_nop 0
	v_mul_f32_e32 v63, v73, v31
	v_mul_f32_e32 v65, 0xbfb8aa3b, v42
	v_exp_f32_e32 v70, v65
	v_mul_f32_e32 v65, 0xbfb8aa3b, v43
	v_exp_f32_e32 v71, v65
	v_rcp_f32_e32 v31, v64
	s_nop 0
	v_mul_f32_e32 v62, v72, v31
	v_pk_mul_f32 v[32:33], v[32:33], v[62:63]
	v_pk_add_f32 v[62:63], v[70:71], 1.0 op_sel_hi:[1,0]
	v_pk_mul_f32 v[32:33], v[32:33], v[130:131] op_sel_hi:[1,0]
	v_cvt_pk_bf16_f32 v31, v32, v33
	global_store_dwordx2 v[132:133], v[30:31], off offset:64
	v_rcp_f32_e32 v30, v63
	s_nop 0
	v_mul_f32_e32 v31, v43, v30
	v_mul_f32_e32 v32, 0xbfb8aa3b, v44
	v_mul_f32_e32 v33, 0xbfb8aa3b, v45
	v_exp_f32_e32 v32, v32
	v_exp_f32_e32 v33, v33
	v_rcp_f32_e32 v30, v62
	s_nop 0
	v_mul_f32_e32 v30, v42, v30
	v_pk_mul_f32 v[10:11], v[10:11], v[30:31]
	v_pk_add_f32 v[32:33], v[32:33], 1.0 op_sel_hi:[1,0]
	v_pk_mul_f32 v[10:11], v[10:11], v[130:131] op_sel_hi:[1,0]
	v_cvt_pk_bf16_f32 v10, v10, v11
	v_rcp_f32_e32 v11, v33
	s_nop 0
	v_mul_f32_e32 v31, v45, v11
	v_rcp_f32_e32 v11, v32
	s_nop 0
	v_mul_f32_e32 v30, v44, v11
	v_pk_mul_f32 v[12:13], v[12:13], v[30:31]
	s_nop 0
	v_pk_mul_f32 v[12:13], v[12:13], v[130:131] op_sel_hi:[1,0]
	s_nop 0
	v_cvt_pk_bf16_f32 v11, v12, v13
	global_store_dwordx2 v[132:133], v[10:11], off offset:96
.LBB0_893:
	s_or_b64 exec, exec, s[46:47]
	v_or_b32_e32 v10, 16, v131
	v_add_u32_e32 v12, s48, v10
	v_cmp_gt_i32_e32 vcc, s65, v12
	s_and_b64 s[10:11], s[44:45], vcc
	s_and_saveexec_b64 s[44:45], s[10:11]
	s_cbranch_execz .LBB0_895
	s_add_i32 s99, s99, 4
	v_ashrrev_i32_e32 v13, 31, v12
	v_lshl_add_u64 v[10:11], v[12:13], 2, s[26:27]
	v_mul_f32_e32 v11, 0xbfb8aa3b, v74
	v_mul_f32_e32 v31, 0xbfb8aa3b, v75
	v_exp_f32_e32 v30, v11
	v_exp_f32_e32 v31, v31
	v_mul_f32_e32 v32, 0xbfb8aa3b, v76
	v_mul_f32_e32 v33, 0xbfb8aa3b, v77
	v_exp_f32_e32 v32, v32
	v_exp_f32_e32 v33, v33
	v_pk_add_f32 v[30:31], v[30:31], 1.0 op_sel_hi:[1,0]
	v_mul_f32_e32 v42, 0xbfb8aa3b, v46
	v_pk_add_f32 v[32:33], v[32:33], 1.0 op_sel_hi:[1,0]
	v_mul_f32_e32 v43, 0xbfb8aa3b, v47
	v_exp_f32_e32 v42, v42
	v_exp_f32_e32 v43, v43
	v_rcp_f32_e32 v11, v31
	s_nop 0
	v_mul_f32_e32 v31, v75, v11
	v_rcp_f32_e32 v11, v30
	s_nop 0
	v_mul_f32_e32 v30, v74, v11
	v_pk_add_f32 v[42:43], v[42:43], 1.0 op_sel_hi:[1,0]
	v_pk_mul_f32 v[30:31], v[54:55], v[30:31]
	v_rcp_f32_e32 v11, v33
	s_nop 0
	v_mul_f32_e32 v33, v77, v11
	v_add_u32_e32 v12, s63, v12
	v_rcp_f32_e32 v11, v32
	s_nop 0
	v_mul_f32_e32 v32, v76, v11
	v_ashrrev_i32_e32 v13, 31, v12
	v_lshlrev_b64 v[12:13], 9, v[12:13]
	v_pk_mul_f32 v[32:33], v[56:57], v[32:33]
	v_lshl_add_u64 v[12:13], s[20:21], 0, v[12:13]
	v_lshl_add_u64 v[12:13], v[12:13], 0, v[162:163]
	v_mov_b32_e32 v10, v245
	v_pk_mul_f32 v[30:31], v[30:31], v[10:11] op_sel_hi:[1,0]
	v_pk_mul_f32 v[32:33], v[32:33], v[10:11] op_sel_hi:[1,0]
	v_cvt_pk_bf16_f32 v30, v30, v31
	v_cvt_pk_bf16_f32 v31, v32, v33
	global_store_dwordx2 v[12:13], v[30:31], off
	v_rcp_f32_e32 v11, v43
	s_nop 0
	v_mul_f32_e32 v31, v47, v11
	v_mul_f32_e32 v30, 0xbfb8aa3b, v48
	v_exp_f32_e32 v32, v30
	v_mul_f32_e32 v30, 0xbfb8aa3b, v49
	v_exp_f32_e32 v33, v30
	v_rcp_f32_e32 v11, v42
	s_nop 0
	v_mul_f32_e32 v30, v46, v11
	v_pk_mul_f32 v[30:31], v[34:35], v[30:31]
	v_pk_add_f32 v[32:33], v[32:33], 1.0 op_sel_hi:[1,0]
	s_nop 0
	v_pk_mul_f32 v[30:31], v[30:31], v[10:11] op_sel_hi:[1,0]
	s_nop 0
	v_cvt_pk_bf16_f32 v30, v30, v31
	v_rcp_f32_e32 v11, v33
	s_nop 0
	v_mul_f32_e32 v33, v49, v11
	v_mul_f32_e32 v31, 0xbfb8aa3b, v18
	v_exp_f32_e32 v34, v31
	v_mul_f32_e32 v31, 0xbfb8aa3b, v19
	v_exp_f32_e32 v35, v31
	v_rcp_f32_e32 v11, v32
	s_nop 0
	v_mul_f32_e32 v32, v48, v11
	v_pk_mul_f32 v[32:33], v[36:37], v[32:33]
	v_pk_add_f32 v[34:35], v[34:35], 1.0 op_sel_hi:[1,0]
	s_nop 0
	v_pk_mul_f32 v[32:33], v[32:33], v[10:11] op_sel_hi:[1,0]
	s_nop 0
	v_cvt_pk_bf16_f32 v31, v32, v33
	global_store_dwordx2 v[12:13], v[30:31], off offset:32
	v_rcp_f32_e32 v11, v35
	s_nop 0
	v_mul_f32_e32 v19, v19, v11
	v_mul_f32_e32 v30, 0xbfb8aa3b, v20
	v_mul_f32_e32 v31, 0xbfb8aa3b, v21
	v_exp_f32_e32 v30, v30
	v_exp_f32_e32 v31, v31
	v_rcp_f32_e32 v11, v34
	s_nop 0
	v_mul_f32_e32 v18, v18, v11
	v_pk_mul_f32 v[14:15], v[14:15], v[18:19]
	v_pk_add_f32 v[30:31], v[30:31], 1.0 op_sel_hi:[1,0]
	s_nop 0
	v_pk_mul_f32 v[14:15], v[14:15], v[10:11] op_sel_hi:[1,0]
	s_nop 0
	v_cvt_pk_bf16_f32 v14, v14, v15
	v_rcp_f32_e32 v11, v31
	s_nop 0
	v_mul_f32_e32 v19, v21, v11
	v_mul_f32_e32 v15, 0xbfb8aa3b, v6
	v_exp_f32_e32 v32, v15
	v_mul_f32_e32 v15, 0xbfb8aa3b, v7
	v_exp_f32_e32 v33, v15
	v_rcp_f32_e32 v11, v30
	s_nop 0
	v_mul_f32_e32 v18, v20, v11
	v_pk_mul_f32 v[16:17], v[16:17], v[18:19]
	v_pk_add_f32 v[18:19], v[32:33], 1.0 op_sel_hi:[1,0]
	s_nop 0
	v_pk_mul_f32 v[16:17], v[16:17], v[10:11] op_sel_hi:[1,0]
	s_nop 0
	v_cvt_pk_bf16_f32 v15, v16, v17
	global_store_dwordx2 v[12:13], v[14:15], off offset:64
	v_rcp_f32_e32 v11, v19
	s_nop 0
	v_mul_f32_e32 v7, v7, v11
	v_mul_f32_e32 v14, 0xbfb8aa3b, v8
	v_mul_f32_e32 v15, 0xbfb8aa3b, v9
	v_exp_f32_e32 v14, v14
	v_exp_f32_e32 v15, v15
	v_rcp_f32_e32 v11, v18
	s_nop 0
	v_mul_f32_e32 v6, v6, v11
	v_pk_mul_f32 v[2:3], v[2:3], v[6:7]
	v_pk_add_f32 v[14:15], v[14:15], 1.0 op_sel_hi:[1,0]
	s_nop 0
	v_pk_mul_f32 v[2:3], v[2:3], v[10:11] op_sel_hi:[1,0]
	s_nop 0
	v_cvt_pk_bf16_f32 v2, v2, v3
	v_rcp_f32_e32 v3, v15
	s_nop 0
	v_mul_f32_e32 v7, v9, v3
	v_rcp_f32_e32 v3, v14
	s_nop 0
	v_mul_f32_e32 v6, v8, v3
	v_pk_mul_f32 v[4:5], v[4:5], v[6:7]
	s_nop 0
	v_pk_mul_f32 v[4:5], v[4:5], v[10:11] op_sel_hi:[1,0]
	s_nop 0
	v_cvt_pk_bf16_f32 v3, v4, v5
	global_store_dwordx2 v[12:13], v[2:3], off offset:96
.LBB0_895:
	s_or_b64 exec, exec, s[44:45]
	v_or_b32_e32 v2, 32, v131
	v_add_u32_e32 v4, s48, v2
	v_cmp_gt_i32_e32 vcc, s65, v4
	s_and_b64 s[10:11], s[42:43], vcc
	s_and_saveexec_b64 s[42:43], s[10:11]
	s_cbranch_execz .LBB0_897
	s_add_i32 s99, s99, 4
	v_ashrrev_i32_e32 v5, 31, v4
	v_lshl_add_u64 v[2:3], v[4:5], 2, s[26:27]
	v_mul_f32_e32 v3, 0xbfb8aa3b, v78
	v_mul_f32_e32 v7, 0xbfb8aa3b, v79
	v_exp_f32_e32 v6, v3
	v_exp_f32_e32 v7, v7
	v_mul_f32_e32 v8, 0xbfb8aa3b, v80
	v_mul_f32_e32 v9, 0xbfb8aa3b, v81
	v_exp_f32_e32 v8, v8
	v_exp_f32_e32 v9, v9
	v_pk_add_f32 v[6:7], v[6:7], 1.0 op_sel_hi:[1,0]
	v_mul_f32_e32 v10, 0xbfb8aa3b, v58
	v_pk_add_f32 v[8:9], v[8:9], 1.0 op_sel_hi:[1,0]
	v_mul_f32_e32 v11, 0xbfb8aa3b, v59
	v_exp_f32_e32 v10, v10
	v_exp_f32_e32 v11, v11
	v_rcp_f32_e32 v3, v7
	s_nop 0
	v_mul_f32_e32 v7, v79, v3
	v_rcp_f32_e32 v3, v6
	s_nop 0
	v_mul_f32_e32 v6, v78, v3
	v_pk_add_f32 v[10:11], v[10:11], 1.0 op_sel_hi:[1,0]
	v_pk_mul_f32 v[6:7], v[82:83], v[6:7]
	v_rcp_f32_e32 v3, v9
	s_nop 0
	v_mul_f32_e32 v9, v81, v3
	v_add_u32_e32 v4, s63, v4
	v_rcp_f32_e32 v3, v8
	s_nop 0
	v_mul_f32_e32 v8, v80, v3
	v_ashrrev_i32_e32 v5, 31, v4
	v_lshlrev_b64 v[4:5], 9, v[4:5]
	v_pk_mul_f32 v[8:9], v[84:85], v[8:9]
	v_lshl_add_u64 v[4:5], s[20:21], 0, v[4:5]
	v_lshl_add_u64 v[4:5], v[4:5], 0, v[162:163]
	v_mov_b32_e32 v2, v246
	v_pk_mul_f32 v[6:7], v[6:7], v[2:3] op_sel_hi:[1,0]
	v_pk_mul_f32 v[8:9], v[8:9], v[2:3] op_sel_hi:[1,0]
	v_cvt_pk_bf16_f32 v6, v6, v7
	v_cvt_pk_bf16_f32 v7, v8, v9
	global_store_dwordx2 v[4:5], v[6:7], off
	v_rcp_f32_e32 v3, v11
	s_nop 0
	v_mul_f32_e32 v7, v59, v3
	v_mul_f32_e32 v6, 0xbfb8aa3b, v60
	v_exp_f32_e32 v8, v6
	v_mul_f32_e32 v6, 0xbfb8aa3b, v61
	v_exp_f32_e32 v9, v6
	v_rcp_f32_e32 v3, v10
	s_nop 0
	v_mul_f32_e32 v6, v58, v3
	v_pk_mul_f32 v[6:7], v[66:67], v[6:7]
	v_pk_add_f32 v[8:9], v[8:9], 1.0 op_sel_hi:[1,0]
	s_nop 0
	v_pk_mul_f32 v[6:7], v[6:7], v[2:3] op_sel_hi:[1,0]
	s_nop 0
	v_cvt_pk_bf16_f32 v6, v6, v7
	v_rcp_f32_e32 v3, v9
	s_nop 0
	v_mul_f32_e32 v9, v61, v3
	v_mul_f32_e32 v7, 0xbfb8aa3b, v38
	v_exp_f32_e32 v10, v7
	v_mul_f32_e32 v7, 0xbfb8aa3b, v39
	v_exp_f32_e32 v11, v7
	v_rcp_f32_e32 v3, v8
	s_nop 0
	v_mul_f32_e32 v8, v60, v3
	v_pk_mul_f32 v[8:9], v[68:69], v[8:9]
	v_pk_add_f32 v[10:11], v[10:11], 1.0 op_sel_hi:[1,0]
	s_nop 0
	v_pk_mul_f32 v[8:9], v[8:9], v[2:3] op_sel_hi:[1,0]
	s_nop 0
	v_cvt_pk_bf16_f32 v7, v8, v9
	global_store_dwordx2 v[4:5], v[6:7], off offset:32
	v_rcp_f32_e32 v3, v11
	s_nop 0
	v_mul_f32_e32 v7, v39, v3
	v_mul_f32_e32 v6, 0xbfb8aa3b, v40
	v_exp_f32_e32 v8, v6
	v_mul_f32_e32 v6, 0xbfb8aa3b, v41
	v_exp_f32_e32 v9, v6
	v_rcp_f32_e32 v3, v10
	s_nop 0
	v_mul_f32_e32 v6, v38, v3
	v_pk_mul_f32 v[6:7], v[50:51], v[6:7]
	v_pk_add_f32 v[8:9], v[8:9], 1.0 op_sel_hi:[1,0]
	s_nop 0
	v_pk_mul_f32 v[6:7], v[6:7], v[2:3] op_sel_hi:[1,0]
	s_nop 0
	v_cvt_pk_bf16_f32 v6, v6, v7
	v_rcp_f32_e32 v3, v9
	s_nop 0
	v_mul_f32_e32 v9, v41, v3
	v_mul_f32_e32 v7, 0xbfb8aa3b, v22
	v_exp_f32_e32 v10, v7
	v_mul_f32_e32 v7, 0xbfb8aa3b, v23
	v_exp_f32_e32 v11, v7
	v_rcp_f32_e32 v3, v8
	s_nop 0
	v_mul_f32_e32 v8, v40, v3
	v_pk_mul_f32 v[8:9], v[52:53], v[8:9]
	v_pk_add_f32 v[10:11], v[10:11], 1.0 op_sel_hi:[1,0]
	s_nop 0
	v_pk_mul_f32 v[8:9], v[8:9], v[2:3] op_sel_hi:[1,0]
	s_nop 0
	v_cvt_pk_bf16_f32 v7, v8, v9
	global_store_dwordx2 v[4:5], v[6:7], off offset:64
	v_rcp_f32_e32 v3, v11
	s_nop 0
	v_mul_f32_e32 v7, v23, v3
	v_mul_f32_e32 v6, 0xbfb8aa3b, v24
	v_exp_f32_e32 v8, v6
	v_mul_f32_e32 v6, 0xbfb8aa3b, v25
	v_exp_f32_e32 v9, v6
	v_rcp_f32_e32 v3, v10
	s_nop 0
	v_mul_f32_e32 v6, v22, v3
	v_pk_mul_f32 v[6:7], v[26:27], v[6:7]
	v_pk_add_f32 v[8:9], v[8:9], 1.0 op_sel_hi:[1,0]
	s_nop 0
	v_pk_mul_f32 v[6:7], v[6:7], v[2:3] op_sel_hi:[1,0]
	s_nop 0
	v_cvt_pk_bf16_f32 v6, v6, v7
	v_rcp_f32_e32 v3, v9
	s_nop 0
	v_mul_f32_e32 v9, v25, v3
	v_rcp_f32_e32 v3, v8
	s_nop 0
	v_mul_f32_e32 v8, v24, v3
	v_pk_mul_f32 v[8:9], v[28:29], v[8:9]
	s_nop 0
	v_pk_mul_f32 v[2:3], v[8:9], v[2:3] op_sel_hi:[1,0]
	s_nop 0
	v_cvt_pk_bf16_f32 v7, v2, v3
	global_store_dwordx2 v[4:5], v[6:7], off offset:96
.LBB0_897:
	s_or_b64 exec, exec, s[42:43]
	v_or_b32_e32 v2, 48, v131
	v_add_u32_e32 v4, s48, v2
	v_cmp_gt_i32_e32 vcc, s65, v4
	s_and_b64 s[10:11], s[40:41], vcc
	s_and_saveexec_b64 s[40:41], s[10:11]
	s_cbranch_execz .LBB0_868
	s_add_i32 s99, s99, 4
	v_ashrrev_i32_e32 v5, 31, v4
	v_lshl_add_u64 v[2:3], v[4:5], 2, s[26:27]
	v_mul_f32_e32 v3, 0xbfb8aa3b, v122
	v_mul_f32_e32 v7, 0xbfb8aa3b, v123
	v_exp_f32_e32 v6, v3
	v_exp_f32_e32 v7, v7
	v_mul_f32_e32 v8, 0xbfb8aa3b, v124
	v_mul_f32_e32 v9, 0xbfb8aa3b, v125
	v_exp_f32_e32 v8, v8
	v_exp_f32_e32 v9, v9
	v_pk_add_f32 v[6:7], v[6:7], 1.0 op_sel_hi:[1,0]
	v_mul_f32_e32 v10, 0xbfb8aa3b, v114
	v_pk_add_f32 v[8:9], v[8:9], 1.0 op_sel_hi:[1,0]
	v_mul_f32_e32 v11, 0xbfb8aa3b, v115
	v_exp_f32_e32 v10, v10
	v_exp_f32_e32 v11, v11
	v_rcp_f32_e32 v3, v7
	s_nop 0
	v_mul_f32_e32 v7, v123, v3
	v_rcp_f32_e32 v3, v6
	s_nop 0
	v_mul_f32_e32 v6, v122, v3
	v_pk_add_f32 v[10:11], v[10:11], 1.0 op_sel_hi:[1,0]
	v_pk_mul_f32 v[6:7], v[126:127], v[6:7]
	v_rcp_f32_e32 v3, v9
	s_nop 0
	v_mul_f32_e32 v9, v125, v3
	v_add_u32_e32 v4, s63, v4
	v_rcp_f32_e32 v3, v8
	s_nop 0
	v_mul_f32_e32 v8, v124, v3
	v_ashrrev_i32_e32 v5, 31, v4
	v_lshlrev_b64 v[4:5], 9, v[4:5]
	v_pk_mul_f32 v[8:9], v[128:129], v[8:9]
	v_lshl_add_u64 v[4:5], s[20:21], 0, v[4:5]
	v_lshl_add_u64 v[4:5], v[4:5], 0, v[162:163]
	v_mov_b32_e32 v2, v247
	v_pk_mul_f32 v[6:7], v[6:7], v[2:3] op_sel_hi:[1,0]
	v_pk_mul_f32 v[8:9], v[8:9], v[2:3] op_sel_hi:[1,0]
	v_cvt_pk_bf16_f32 v6, v6, v7
	v_cvt_pk_bf16_f32 v7, v8, v9
	global_store_dwordx2 v[4:5], v[6:7], off
	v_rcp_f32_e32 v3, v11
	s_nop 0
	v_mul_f32_e32 v7, v115, v3
	v_mul_f32_e32 v6, 0xbfb8aa3b, v116
	v_exp_f32_e32 v8, v6
	v_mul_f32_e32 v6, 0xbfb8aa3b, v117
	v_exp_f32_e32 v9, v6
	v_rcp_f32_e32 v3, v10
	s_nop 0
	v_mul_f32_e32 v6, v114, v3
	v_pk_mul_f32 v[6:7], v[118:119], v[6:7]
	v_pk_add_f32 v[8:9], v[8:9], 1.0 op_sel_hi:[1,0]
	s_nop 0
	v_pk_mul_f32 v[6:7], v[6:7], v[2:3] op_sel_hi:[1,0]
	s_nop 0
	v_cvt_pk_bf16_f32 v6, v6, v7
	v_rcp_f32_e32 v3, v9
	s_nop 0
	v_mul_f32_e32 v9, v117, v3
	v_mul_f32_e32 v7, 0xbfb8aa3b, v106
	v_exp_f32_e32 v10, v7
	v_mul_f32_e32 v7, 0xbfb8aa3b, v107
	v_exp_f32_e32 v11, v7
	v_rcp_f32_e32 v3, v8
	s_nop 0
	v_mul_f32_e32 v8, v116, v3
	v_pk_mul_f32 v[8:9], v[120:121], v[8:9]
	v_pk_add_f32 v[10:11], v[10:11], 1.0 op_sel_hi:[1,0]
	s_nop 0
	v_pk_mul_f32 v[8:9], v[8:9], v[2:3] op_sel_hi:[1,0]
	s_nop 0
	v_cvt_pk_bf16_f32 v7, v8, v9
	global_store_dwordx2 v[4:5], v[6:7], off offset:32
	v_rcp_f32_e32 v3, v11
	s_nop 0
	v_mul_f32_e32 v7, v107, v3
	v_mul_f32_e32 v6, 0xbfb8aa3b, v108
	v_exp_f32_e32 v8, v6
	v_mul_f32_e32 v6, 0xbfb8aa3b, v109
	v_exp_f32_e32 v9, v6
	v_rcp_f32_e32 v3, v10
	s_nop 0
	v_mul_f32_e32 v6, v106, v3
	v_pk_mul_f32 v[6:7], v[110:111], v[6:7]
	v_pk_add_f32 v[8:9], v[8:9], 1.0 op_sel_hi:[1,0]
	s_nop 0
	v_pk_mul_f32 v[6:7], v[6:7], v[2:3] op_sel_hi:[1,0]
	s_nop 0
	v_cvt_pk_bf16_f32 v6, v6, v7
	v_rcp_f32_e32 v3, v9
	s_nop 0
	v_mul_f32_e32 v9, v109, v3
	v_mul_f32_e32 v7, 0xbfb8aa3b, v102
	v_exp_f32_e32 v10, v7
	v_mul_f32_e32 v7, 0xbfb8aa3b, v103
	v_exp_f32_e32 v11, v7
	v_rcp_f32_e32 v3, v8
	s_nop 0
	v_mul_f32_e32 v8, v108, v3
	v_pk_mul_f32 v[8:9], v[112:113], v[8:9]
	v_pk_add_f32 v[10:11], v[10:11], 1.0 op_sel_hi:[1,0]
	s_nop 0
	v_pk_mul_f32 v[8:9], v[8:9], v[2:3] op_sel_hi:[1,0]
	s_nop 0
	v_cvt_pk_bf16_f32 v7, v8, v9
	global_store_dwordx2 v[4:5], v[6:7], off offset:64
	v_rcp_f32_e32 v3, v11
	s_nop 0
	v_mul_f32_e32 v7, v103, v3
	v_mul_f32_e32 v6, 0xbfb8aa3b, v104
	v_exp_f32_e32 v8, v6
	v_mul_f32_e32 v6, 0xbfb8aa3b, v105
	v_exp_f32_e32 v9, v6
	v_rcp_f32_e32 v3, v10
	s_nop 0
	v_mul_f32_e32 v6, v102, v3
	v_pk_mul_f32 v[6:7], v[98:99], v[6:7]
	v_pk_add_f32 v[8:9], v[8:9], 1.0 op_sel_hi:[1,0]
	s_nop 0
	v_pk_mul_f32 v[6:7], v[6:7], v[2:3] op_sel_hi:[1,0]
	s_nop 0
	v_cvt_pk_bf16_f32 v6, v6, v7
	v_rcp_f32_e32 v3, v9
	s_nop 0
	v_mul_f32_e32 v9, v105, v3
	v_rcp_f32_e32 v3, v8
	s_nop 0
	v_mul_f32_e32 v8, v104, v3
	v_pk_mul_f32 v[8:9], v[100:101], v[8:9]
	s_nop 0
	v_pk_mul_f32 v[2:3], v[8:9], v[2:3] op_sel_hi:[1,0]
	s_nop 0
	v_cvt_pk_bf16_f32 v7, v2, v3
	global_store_dwordx2 v[4:5], v[6:7], off offset:96
	s_branch .LBB0_868
